# rwkv chunk algebra: the three interleaved load/MFMA sequences (A_br, A_ak, A_kr) now issue their 16 fragment loads up front (register renaming), one memory round trip each instead of ~10
# baseline (speedup 1.0000x reference)
; #define R2_ZERO(M) do { _Pragma("unroll") for (int _a = 0; _a < 2; ++_a) _Pragma("unroll") for (int _b = 0; _b < 2; ++_b) _Pragma("unroll") for (int _r = 0; _r < 16; ++_r) M[_a][_b][_r] = 0.f; } while (0)
; #define R2_PACK(Bpk, M) do { _Pragma("unroll") for (int _ks = 0; _ks < 4; ++_ks) _Pragma("unroll") for (int _cb = 0; _cb < 2; ++_cb) Bpk[_ks][_cb] = pack_acc(M[_ks >> 1][_cb], _ks & 1); } while (0)
; __device__ __forceinline__ void ph_rwkv_chunk(const Params& p, int l, LAS unsigned char* lds, const int wvid) {
;     ...
;             for (int it = 0; it < 5; ++it) {
;                 { M64 A2; R2_ZERO(A2); R2_MM_LP(A2, X, Apk);
;                   asm volatile("" ::: "memory");
;                   R2_TO_LDS(X, A2); R2_PACK(Apk, A2); }
;                 R2_PACK(Tpk, Tm);
;                 R2_MM_LP(Tm, X, Tpk);
;                 asm volatile("" ::: "memory");
;             }
.LBB0_651:
	ds_read_b128 v[66:69], v225
	s_nop 4
	v_cvt_pk_bf16_f32 v166, v34, v35
	v_cvt_pk_bf16_f32 v167, v36, v37
	v_cvt_pk_bf16_f32 v168, v38, v39
	v_cvt_pk_bf16_f32 v169, v40, v41
	v_cvt_pk_bf16_f32 v162, v2, v3
	v_cvt_pk_bf16_f32 v163, v4, v5
	v_cvt_pk_bf16_f32 v164, v6, v7
	v_cvt_pk_bf16_f32 v165, v8, v9
	s_waitcnt lgkmcnt(0)
	v_mfma_f32_32x32x16_bf16 v[114:129], v[66:69], v[142:145], 0
	v_cvt_pk_bf16_f32 v170, v42, v43
	v_cvt_pk_bf16_f32 v171, v44, v45
	v_cvt_pk_bf16_f32 v172, v46, v47
	v_cvt_pk_bf16_f32 v173, v48, v49
	v_cvt_pk_bf16_f32 v174, v10, v11
	v_cvt_pk_bf16_f32 v175, v12, v13
	v_cvt_pk_bf16_f32 v176, v14, v15
	v_mfma_f32_32x32x16_bf16 v[98:113], v[66:69], v[154:157], 0
	ds_read_b128 v[66:69], v225 offset:4608
	v_cvt_pk_bf16_f32 v177, v16, v17
	v_cvt_pk_bf16_f32 v178, v50, v51
	v_cvt_pk_bf16_f32 v179, v52, v53
	v_cvt_pk_bf16_f32 v180, v54, v55
	v_cvt_pk_bf16_f32 v181, v56, v57
	s_add_i32 s40, s40, -1
	s_waitcnt lgkmcnt(0)
	v_mfma_f32_32x32x16_bf16 v[82:97], v[66:69], v[142:145], 0
	ds_read_b128 v[142:145], v225 offset:32
	s_cmp_lg_u32 s40, 0
	s_waitcnt lgkmcnt(0)
	v_mfma_f32_32x32x16_bf16 v[114:129], v[142:145], v[138:141], v[114:129]
	v_mfma_f32_32x32x16_bf16 v[98:113], v[142:145], v[146:149], v[98:113]
	ds_read_b128 v[142:145], v225 offset:4640
	s_waitcnt lgkmcnt(0)
	v_mfma_f32_32x32x16_bf16 v[82:97], v[142:145], v[138:141], v[82:97]
	ds_read_b128 v[138:141], v225 offset:64
	v_mfma_f32_32x32x16_bf16 v[66:81], v[66:69], v[154:157], 0
	s_waitcnt lgkmcnt(0)
	v_mfma_f32_32x32x16_bf16 v[114:129], v[138:141], v[158:161], v[114:129]
	v_mfma_f32_32x32x16_bf16 v[98:113], v[138:141], v[150:153], v[98:113]
	ds_read_b128 v[138:141], v225 offset:4672
	v_mfma_f32_32x32x16_bf16 v[66:81], v[142:145], v[146:149], v[66:81]
	s_waitcnt lgkmcnt(0)
	v_mfma_f32_32x32x16_bf16 v[82:97], v[138:141], v[158:161], v[82:97]
	v_mfma_f32_32x32x16_bf16 v[66:81], v[138:141], v[150:153], v[66:81]
	ds_read_b128 v[138:141], v225 offset:96
	s_waitcnt lgkmcnt(0)
	v_mfma_f32_32x32x16_bf16 v[114:129], v[138:141], v[134:137], v[114:129]
	v_mfma_f32_32x32x16_bf16 v[98:113], v[138:141], v[130:133], v[98:113]
	ds_read_b128 v[138:141], v225 offset:4704
	s_nop 9
	v_cvt_pk_bf16_f32 v142, v114, v115
	v_cvt_pk_bf16_f32 v143, v116, v117
	v_cvt_pk_bf16_f32 v144, v118, v119
	v_cvt_pk_bf16_f32 v145, v120, v121
	s_waitcnt lgkmcnt(0)
	v_mfma_f32_32x32x16_bf16 v[82:97], v[138:141], v[134:137], v[82:97]
	v_cvt_pk_bf16_f32 v154, v98, v99
	v_cvt_pk_bf16_f32 v155, v100, v101
	v_cvt_pk_bf16_f32 v156, v102, v103
	v_cvt_pk_bf16_f32 v157, v104, v105
	v_cvt_pk_bf16_f32 v146, v106, v107
	v_cvt_pk_bf16_f32 v147, v108, v109
	v_cvt_pk_bf16_f32 v148, v110, v111
	v_mfma_f32_32x32x16_bf16 v[66:81], v[138:141], v[130:133], v[66:81]
	v_cvt_pk_bf16_f32 v138, v122, v123
	v_cvt_pk_bf16_f32 v139, v124, v125
	v_cvt_pk_bf16_f32 v140, v126, v127
	v_cvt_pk_bf16_f32 v141, v128, v129
	v_cvt_pk_bf16_f32 v149, v112, v113
	v_cvt_pk_bf16_f32 v158, v82, v83
	v_cvt_pk_bf16_f32 v159, v84, v85
	v_cvt_pk_bf16_f32 v160, v86, v87
	v_cvt_pk_bf16_f32 v161, v88, v89
	v_cvt_pk_bf16_f32 v134, v90, v91
	v_cvt_pk_bf16_f32 v135, v92, v93
	v_cvt_pk_bf16_f32 v136, v94, v95
	v_cvt_pk_bf16_f32 v137, v96, v97
	v_cvt_pk_bf16_f32 v150, v66, v67
	v_cvt_pk_bf16_f32 v151, v68, v69
	v_cvt_pk_bf16_f32 v152, v70, v71
	v_cvt_pk_bf16_f32 v153, v72, v73
	v_cvt_pk_bf16_f32 v130, v74, v75
	v_cvt_pk_bf16_f32 v131, v76, v77
	v_cvt_pk_bf16_f32 v132, v78, v79
	v_cvt_pk_bf16_f32 v133, v80, v81
	ds_write_b16 v194, v142
	ds_write_b16_d16_hi v194, v142 offset:144
	ds_write_b16 v224, v143
	ds_write_b16_d16_hi v224, v143 offset:144
	ds_write_b16 v223, v144
	ds_write_b16_d16_hi v223, v144 offset:144
	ds_write_b16 v199, v145
	ds_write_b16_d16_hi v199, v145 offset:144
	ds_write_b16 v198, v138
	ds_write_b16_d16_hi v198, v138 offset:144
	ds_write_b16 v197, v139
	ds_write_b16_d16_hi v197, v139 offset:144
	ds_write_b16 v196, v140
	ds_write_b16_d16_hi v196, v140 offset:144
	ds_write_b16 v195, v141
	ds_write_b16_d16_hi v195, v141 offset:144
	ds_write_b16 v194, v154 offset:64
	ds_write_b16_d16_hi v194, v154 offset:208
	ds_write_b16 v224, v155 offset:64
	ds_write_b16_d16_hi v224, v155 offset:208
	ds_write_b16 v223, v156 offset:64
	ds_write_b16_d16_hi v223, v156 offset:208
	ds_write_b16 v199, v157 offset:64
	ds_write_b16_d16_hi v199, v157 offset:208
	ds_write_b16 v198, v146 offset:64
	ds_write_b16_d16_hi v198, v146 offset:208
	ds_write_b16 v197, v147 offset:64
	ds_write_b16_d16_hi v197, v147 offset:208
	ds_write_b16 v196, v148 offset:64
	ds_write_b16_d16_hi v196, v148 offset:208
	ds_write_b16 v195, v149 offset:64
	ds_write_b16_d16_hi v195, v149 offset:208
	ds_write_b16 v194, v158 offset:4608
	ds_write_b16_d16_hi v194, v158 offset:4752
	ds_write_b16 v193, v159
	ds_write_b16_d16_hi v193, v159 offset:144
	ds_write_b16 v193, v160 offset:864
	ds_write_b16_d16_hi v193, v160 offset:1008
	ds_write_b16 v193, v161 offset:1152
	ds_write_b16_d16_hi v193, v161 offset:1296
	ds_write_b16 v193, v134 offset:2016
	ds_write_b16_d16_hi v193, v134 offset:2160
	ds_write_b16 v193, v135 offset:2304
	ds_write_b16_d16_hi v193, v135 offset:2448
	ds_write_b16 v193, v136 offset:3168
	ds_write_b16_d16_hi v193, v136 offset:3312
	ds_write_b16 v193, v137 offset:3456
	ds_write_b16_d16_hi v193, v137 offset:3600
	ds_write_b16 v194, v150 offset:4672
	ds_write_b16_d16_hi v194, v150 offset:4816
	ds_write_b16 v193, v151 offset:64
	ds_write_b16_d16_hi v193, v151 offset:208
	ds_write_b16 v193, v152 offset:928
	ds_write_b16_d16_hi v193, v152 offset:1072
	ds_write_b16 v193, v153 offset:1216
	ds_write_b16_d16_hi v193, v153 offset:1360
	ds_write_b16 v193, v130 offset:2080
	ds_write_b16_d16_hi v193, v130 offset:2224
	ds_write_b16 v193, v131 offset:2368
	ds_write_b16_d16_hi v193, v131 offset:2512
	ds_write_b16 v193, v132 offset:3232
	ds_write_b16_d16_hi v193, v132 offset:3376
	ds_write_b16 v193, v133 offset:3520
	ds_write_b16_d16_hi v193, v133 offset:3664
	ds_read_b128 v[66:69], v225
	s_waitcnt lgkmcnt(0)
; #define R2_PACK(Bpk, M) do { _Pragma("unroll") for (int _ks = 0; _ks < 4; ++_ks) _Pragma("unroll") for (int _cb = 0; _cb < 2; ++_cb) Bpk[_ks][_cb] = pack_acc(M[_ks >> 1][_cb], _ks & 1); } while (0)
; __device__ __forceinline__ void ph_rwkv_chunk(const Params& p, int l, LAS unsigned char* lds, const int wvid) {
;     ...
;                 R2_MM_LP(Tm, X, Tpk);
;                 asm volatile("" ::: "memory");
;             }
;             R2_PACK(Tpk, Tm);
;         }
;         {
;             R2_RAW(X, ATg); R2_TRANS_L(Y, X);
	v_mfma_f32_32x32x16_bf16 v[34:49], v[66:69], v[166:169], v[34:49]
	v_cvt_pk_bf16_f32 v70, v18, v19
	v_cvt_pk_bf16_f32 v74, v58, v59
	v_cvt_pk_bf16_f32 v75, v60, v61
	v_cvt_pk_bf16_f32 v76, v62, v63
	v_cvt_pk_bf16_f32 v77, v64, v65
	v_cvt_pk_bf16_f32 v71, v20, v21
	v_cvt_pk_bf16_f32 v72, v22, v23
	v_mfma_f32_32x32x16_bf16 v[2:17], v[66:69], v[162:165], v[2:17]
	ds_read_b128 v[66:69], v225 offset:4608
	v_cvt_pk_bf16_f32 v73, v24, v25
	v_cvt_pk_bf16_f32 v78, v26, v27
	v_cvt_pk_bf16_f32 v79, v28, v29
	v_cvt_pk_bf16_f32 v80, v30, v31
	v_cvt_pk_bf16_f32 v81, v32, v33
	s_waitcnt lgkmcnt(0)
	v_mfma_f32_32x32x16_bf16 v[50:65], v[66:69], v[166:169], v[50:65]
	v_mfma_f32_32x32x16_bf16 v[18:33], v[66:69], v[162:165], v[18:33]
	ds_read_b128 v[66:69], v225 offset:32
	s_waitcnt lgkmcnt(0)
	v_mfma_f32_32x32x16_bf16 v[34:49], v[66:69], v[170:173], v[34:49]
	v_mfma_f32_32x32x16_bf16 v[2:17], v[66:69], v[174:177], v[2:17]
	ds_read_b128 v[66:69], v225 offset:4640
	s_waitcnt lgkmcnt(0)
	v_mfma_f32_32x32x16_bf16 v[50:65], v[66:69], v[170:173], v[50:65]
	v_mfma_f32_32x32x16_bf16 v[18:33], v[66:69], v[174:177], v[18:33]
	ds_read_b128 v[66:69], v225 offset:64
	s_waitcnt lgkmcnt(0)
	v_mfma_f32_32x32x16_bf16 v[34:49], v[66:69], v[178:181], v[34:49]
	v_mfma_f32_32x32x16_bf16 v[2:17], v[66:69], v[70:73], v[2:17]
	ds_read_b128 v[66:69], v225 offset:4672
	s_waitcnt lgkmcnt(0)
	v_mfma_f32_32x32x16_bf16 v[50:65], v[66:69], v[178:181], v[50:65]
	v_mfma_f32_32x32x16_bf16 v[18:33], v[66:69], v[70:73], v[18:33]
	ds_read_b128 v[66:69], v225 offset:96
	s_waitcnt lgkmcnt(0)
	v_mfma_f32_32x32x16_bf16 v[34:49], v[66:69], v[74:77], v[34:49]
	v_mfma_f32_32x32x16_bf16 v[2:17], v[66:69], v[78:81], v[2:17]
	ds_read_b128 v[66:69], v225 offset:4704
	s_waitcnt lgkmcnt(0)
	v_mfma_f32_32x32x16_bf16 v[50:65], v[66:69], v[74:77], v[50:65]
	v_mfma_f32_32x32x16_bf16 v[18:33], v[66:69], v[78:81], v[18:33]
	s_cbranch_scc1 .LBB0_651
	v_lshlrev_b32_e32 v0, 4, v183
	v_lshl_add_u64 v[82:83], s[86:87], 0, v[0:1]
	s_movk_i32 s44, 0x1000
	v_add_co_u32_e32 v94, vcc, s44, v82
	global_load_dwordx4 v[66:69], v0, s[86:87]
	global_load_dwordx4 v[70:73], v0, s[86:87] offset:1024
	global_load_dwordx4 v[74:77], v0, s[86:87] offset:2048
	global_load_dwordx4 v[78:81], v0, s[86:87] offset:3072
	v_addc_co_u32_e32 v95, vcc, 0, v83, vcc
	global_load_dwordx4 v[82:85], v[94:95], off
	global_load_dwordx4 v[86:89], v[94:95], off offset:1024
	global_load_dwordx4 v[90:93], v[94:95], off offset:2048
	s_nop 0
	global_load_dwordx4 v[94:97], v[94:95], off offset:3072
	v_lshlrev_b32_e32 v0, 4, v182
	v_lshrrev_b32_e32 v98, 1, v183
	v_bfe_u32 v99, v182, 1, 5
	v_and_b32_e32 v0, 16, v0
	v_mul_u32_u24_e32 v98, 0x90, v98
	v_mul_u32_u24_e32 v99, 0x90, v99
	v_add3_u32 v98, s48, v98, v0
	v_add3_u32 v0, s48, v99, v0
	v_lshl_add_u32 v100, v183, 1, s48
	v_mov_b32_e32 v191, s48
	v_mad_u32_u24 v101, v183, s83, v191
	v_cvt_pk_bf16_f32 v166, v2, v3
	v_cvt_pk_bf16_f32 v167, v4, v5
	v_cvt_pk_bf16_f32 v162, v34, v35
	v_cvt_pk_bf16_f32 v163, v36, v37
	v_cvt_pk_bf16_f32 v164, v38, v39
	v_cvt_pk_bf16_f32 v165, v40, v41
	v_cvt_pk_bf16_f32 v168, v6, v7
	v_cvt_pk_bf16_f32 v169, v8, v9
	v_cvt_pk_bf16_f32 v154, v42, v43
	v_cvt_pk_bf16_f32 v155, v44, v45
	v_cvt_pk_bf16_f32 v156, v46, v47
	v_cvt_pk_bf16_f32 v157, v48, v49
	v_cvt_pk_bf16_f32 v158, v10, v11
	v_cvt_pk_bf16_f32 v159, v12, v13
	v_cvt_pk_bf16_f32 v160, v14, v15
	v_cvt_pk_bf16_f32 v161, v16, v17
	v_cvt_pk_bf16_f32 v182, v50, v51
	v_cvt_pk_bf16_f32 v183, v52, v53
	v_cvt_pk_bf16_f32 v184, v54, v55
	v_cvt_pk_bf16_f32 v185, v56, v57
	v_cvt_pk_bf16_f32 v186, v18, v19
	v_cvt_pk_bf16_f32 v187, v20, v21
	v_cvt_pk_bf16_f32 v188, v22, v23
	v_cvt_pk_bf16_f32 v189, v24, v25
	v_cvt_pk_bf16_f32 v178, v58, v59
	v_cvt_pk_bf16_f32 v179, v60, v61
	v_cvt_pk_bf16_f32 v180, v62, v63
	v_cvt_pk_bf16_f32 v181, v64, v65
	v_cvt_pk_bf16_f32 v150, v26, v27
	v_cvt_pk_bf16_f32 v151, v28, v29
	v_cvt_pk_bf16_f32 v152, v30, v31
	v_cvt_pk_bf16_f32 v153, v32, v33
	s_lshl_b64 s[38:39], s[42:43], 1
	s_add_u32 s72, s94, s38
	s_addc_u32 s73, s52, s39
	s_add_u32 s36, s53, s38
	s_addc_u32 s37, s59, s39
	s_add_u32 s54, s46, s38
	s_addc_u32 s55, s77, s39
	s_mov_b32 s42, s41
	s_mov_b32 s43, s41
	s_mov_b32 s40, s41
	s_waitcnt vmcnt(7)
	ds_write_b128 v98, v[66:69]
	s_waitcnt vmcnt(6)
	ds_write_b128 v98, v[70:73] offset:4608
	s_waitcnt vmcnt(5)
	ds_write_b128 v98, v[74:77] offset:32
	s_waitcnt vmcnt(4)
	ds_write_b128 v0, v[78:81] offset:4640
	s_waitcnt vmcnt(3)
	ds_write_b128 v98, v[82:85] offset:64
	s_waitcnt vmcnt(2)
	ds_write_b128 v0, v[86:89] offset:4672
	s_waitcnt vmcnt(1)
	ds_write_b128 v98, v[90:93] offset:96
	s_waitcnt vmcnt(0)
	ds_write_b128 v0, v[94:97] offset:4704
	ds_read_u16 v0, v100
	ds_read_u16 v66, v100 offset:144
	ds_read_u16 v67, v100 offset:288
	ds_read_u16 v68, v100 offset:432
	ds_read_u16 v70, v100 offset:576
	ds_read_u16 v71, v100 offset:720
	ds_read_u16 v72, v100 offset:864
	ds_read_u16 v73, v100 offset:1008
	ds_read_u16 v69, v100 offset:1152
	ds_read_u16 v74, v100 offset:1296
	ds_read_u16 v75, v100 offset:1440
	ds_read_u16 v76, v100 offset:1584
	ds_read_u16 v77, v100 offset:1728
	ds_read_u16 v78, v100 offset:1872
	ds_read_u16 v79, v100 offset:2016
	ds_read_u16 v80, v100 offset:2160
	ds_read_u16 v81, v100 offset:2304
	ds_read_u16 v82, v100 offset:2448
	ds_read_u16 v83, v100 offset:2592
	ds_read_u16 v84, v100 offset:2736
	ds_read_u16 v85, v100 offset:2880
	ds_read_u16 v86, v100 offset:3024
	ds_read_u16 v87, v100 offset:3168
	ds_read_u16 v88, v100 offset:3312
	ds_read_u16 v89, v100 offset:3456
	ds_read_u16 v90, v100 offset:3600
	ds_read_u16 v91, v100 offset:3744
	ds_read_u16 v92, v100 offset:3888
	ds_read_u16 v93, v100 offset:4032
	ds_read_u16 v94, v100 offset:4176
	ds_read_u16 v95, v100 offset:4320
	ds_read_u16 v96, v100 offset:4464
	ds_read_u16 v97, v100 offset:4608
	ds_read_u16 v98, v100 offset:4752
	ds_read_u16 v99, v100 offset:4896
	ds_read_u16 v102, v100 offset:5040
	ds_read_u16 v103, v100 offset:5184
	ds_read_u16 v104, v100 offset:5328
	s_waitcnt lgkmcnt(14)
; #define R2_ZERO(M) do { _Pragma("unroll") for (int _a = 0; _a < 2; ++_a) _Pragma("unroll") for (int _b = 0; _b < 2; ++_b) _Pragma("unroll") for (int _r = 0; _r < 16; ++_r) M[_a][_b][_r] = 0.f; } while (0)
; __device__ __forceinline__ void ph_rwkv_chunk(const Params& p, int l, LAS unsigned char* lds, const int wvid) {
;     ...
;             R2_RAW(X, ATg); R2_TRANS_L(Y, X);
;             M64 W; R2_ZERO(W); R2_MM_LP(W, Y, Tpk);
;             R2_TO_LDS(X, W);
;         }
	v_lshl_or_b32 v66, v66, 16, v0
	v_lshl_or_b32 v67, v68, 16, v67
	v_lshl_or_b32 v68, v74, 16, v69
	v_lshl_or_b32 v69, v76, 16, v75
	v_lshl_or_b32 v70, v71, 16, v70
	v_lshl_or_b32 v71, v73, 16, v72
	v_lshl_or_b32 v72, v78, 16, v77
	v_lshl_or_b32 v73, v80, 16, v79
	v_lshl_or_b32 v74, v82, 16, v81
	v_lshl_or_b32 v75, v84, 16, v83
	s_waitcnt lgkmcnt(12)
	v_lshl_or_b32 v76, v90, 16, v89
	s_waitcnt lgkmcnt(10)
	v_lshl_or_b32 v77, v92, 16, v91
	v_lshl_or_b32 v78, v86, 16, v85
	v_lshl_or_b32 v79, v88, 16, v87
	s_waitcnt lgkmcnt(8)
	v_lshl_or_b32 v80, v94, 16, v93
	s_waitcnt lgkmcnt(6)
	v_lshl_or_b32 v81, v96, 16, v95
	ds_write_b128 v101, v[66:69] offset:9216
	ds_write_b128 v101, v[70:73] offset:9232
	ds_write_b128 v101, v[74:77] offset:9248
	ds_write_b128 v101, v[78:81] offset:9264
	ds_read_u16 v0, v100 offset:5472
	ds_read_u16 v70, v100 offset:5616
	ds_read_u16 v68, v100 offset:5760
	ds_read_u16 v69, v100 offset:5904
	ds_read_u16 v71, v100 offset:6048
	ds_read_u16 v72, v100 offset:6192
	ds_read_u16 v73, v100 offset:6336
	ds_read_u16 v74, v100 offset:6480
	ds_read_u16 v75, v100 offset:6624
	ds_read_u16 v76, v100 offset:6768
	s_waitcnt lgkmcnt(14)
	v_lshl_or_b32 v66, v98, 16, v97
	v_lshl_or_b32 v67, v102, 16, v99
	s_waitcnt lgkmcnt(6)
	v_lshl_or_b32 v68, v69, 16, v68
	s_waitcnt lgkmcnt(4)
	v_lshl_or_b32 v69, v72, 16, v71
	ds_write_b128 v101, v[66:69] offset:9280
	v_lshl_or_b32 v66, v104, 16, v103
	v_lshl_or_b32 v67, v70, 16, v0
	s_waitcnt lgkmcnt(3)
	v_lshl_or_b32 v68, v74, 16, v73
	s_waitcnt lgkmcnt(1)
	v_lshl_or_b32 v69, v76, 16, v75
	ds_write_b128 v101, v[66:69] offset:9296
	ds_read_u16 v0, v100 offset:6912
	ds_read_u16 v66, v100 offset:7056
	ds_read_u16 v67, v100 offset:7200
	ds_read_u16 v68, v100 offset:7344
	ds_read_u16 v70, v100 offset:7488
	ds_read_u16 v71, v100 offset:7632
	ds_read_u16 v72, v100 offset:7776
	ds_read_u16 v73, v100 offset:7920
	s_waitcnt lgkmcnt(6)
	v_lshl_or_b32 v66, v66, 16, v0
	s_waitcnt lgkmcnt(4)
	v_lshl_or_b32 v67, v68, 16, v67
	ds_read_u16 v0, v100 offset:8064
	ds_read_u16 v68, v100 offset:8208
	ds_read_u16 v69, v100 offset:8352
	ds_read_u16 v74, v100 offset:8496
	ds_read_u16 v75, v100 offset:8640
	ds_read_u16 v76, v100 offset:8784
	ds_read_u16 v77, v100 offset:8928
	ds_read_u16 v78, v100 offset:9072
	s_waitcnt lgkmcnt(6)
	v_lshl_or_b32 v68, v68, 16, v0
	s_waitcnt lgkmcnt(4)
	v_lshl_or_b32 v69, v74, 16, v69
	ds_write_b128 v101, v[66:69] offset:9312
	v_lshl_or_b32 v66, v71, 16, v70
	v_lshl_or_b32 v67, v73, 16, v72
	s_waitcnt lgkmcnt(3)
	v_lshl_or_b32 v68, v76, 16, v75
	s_waitcnt lgkmcnt(1)
	v_lshl_or_b32 v69, v78, 16, v77
	ds_write_b128 v101, v[66:69] offset:9328
	ds_read_b128 v[66:69], v225 offset:9216
	ds_read_b128 v[2:5], v225 offset:13824
	s_waitcnt lgkmcnt(1)
	v_mfma_f32_32x32x16_bf16 v[114:129], v[66:69], v[162:165], 0
	v_mfma_f32_32x32x16_bf16 v[98:113], v[66:69], v[166:169], 0
	s_waitcnt lgkmcnt(0)
	v_mfma_f32_32x32x16_bf16 v[82:97], v[2:5], v[162:165], 0
	v_mfma_f32_32x32x16_bf16 v[66:81], v[2:5], v[166:169], 0
	ds_read_b128 v[2:5], v225 offset:9248
	s_waitcnt lgkmcnt(0)
	v_mfma_f32_32x32x16_bf16 v[114:129], v[2:5], v[154:157], v[114:129]
	v_mfma_f32_32x32x16_bf16 v[98:113], v[2:5], v[158:161], v[98:113]
	ds_read_b128 v[2:5], v225 offset:13856
	s_waitcnt lgkmcnt(0)
	v_mfma_f32_32x32x16_bf16 v[82:97], v[2:5], v[154:157], v[82:97]
	v_mfma_f32_32x32x16_bf16 v[66:81], v[2:5], v[158:161], v[66:81]
	ds_read_b128 v[2:5], v225 offset:9280
	s_waitcnt lgkmcnt(0)
	v_mfma_f32_32x32x16_bf16 v[114:129], v[2:5], v[182:185], v[114:129]
	v_mfma_f32_32x32x16_bf16 v[98:113], v[2:5], v[186:189], v[98:113]
	ds_read_b128 v[2:5], v225 offset:13888
	s_waitcnt lgkmcnt(0)
	v_mfma_f32_32x32x16_bf16 v[82:97], v[2:5], v[182:185], v[82:97]
	v_mfma_f32_32x32x16_bf16 v[66:81], v[2:5], v[186:189], v[66:81]
	ds_read_b128 v[2:5], v225 offset:9312
	s_waitcnt lgkmcnt(0)
	v_mfma_f32_32x32x16_bf16 v[114:129], v[2:5], v[178:181], v[114:129]
	v_mfma_f32_32x32x16_bf16 v[98:113], v[2:5], v[150:153], v[98:113]
	ds_read_b128 v[2:5], v225 offset:13920
	s_nop 9
	v_cvt_pk_bf16_f32 v0, v114, v115
	ds_write_b16 v194, v0
	ds_write_b16_d16_hi v194, v0 offset:144
	v_cvt_pk_bf16_f32 v0, v116, v117
	ds_write_b16 v224, v0
	ds_write_b16_d16_hi v224, v0 offset:144
	v_cvt_pk_bf16_f32 v0, v118, v119
	ds_write_b16 v223, v0
	ds_write_b16_d16_hi v223, v0 offset:144
	v_cvt_pk_bf16_f32 v0, v120, v121
	ds_write_b16 v199, v0
	ds_write_b16_d16_hi v199, v0 offset:144
	v_cvt_pk_bf16_f32 v0, v122, v123
	ds_write_b16 v198, v0
	ds_write_b16_d16_hi v198, v0 offset:144
	v_cvt_pk_bf16_f32 v0, v124, v125
	ds_write_b16 v197, v0
	ds_write_b16_d16_hi v197, v0 offset:144
	v_cvt_pk_bf16_f32 v0, v126, v127
	ds_write_b16 v196, v0
	ds_write_b16_d16_hi v196, v0 offset:144
	v_cvt_pk_bf16_f32 v0, v128, v129
	s_waitcnt lgkmcnt(14)
; #define R2_ZERO(M) do { _Pragma("unroll") for (int _a = 0; _a < 2; ++_a) _Pragma("unroll") for (int _b = 0; _b < 2; ++_b) _Pragma("unroll") for (int _r = 0; _r < 16; ++_r) M[_a][_b][_r] = 0.f; } while (0)
; #define R2_PACK(Bpk, M) do { _Pragma("unroll") for (int _ks = 0; _ks < 4; ++_ks) _Pragma("unroll") for (int _cb = 0; _cb < 2; ++_cb) Bpk[_ks][_cb] = pack_acc(M[_ks >> 1][_cb], _ks & 1); } while (0)
; #define R2_MASK(M, STRICT) do { _Pragma("unroll") for (int _rb = 0; _rb < 2; ++_rb) _Pragma("unroll") for (int _cb = 0; _cb < 2; ++_cb) _Pragma("unroll") for (int _r = 0; _r < 16; ++_r) { \
;         const int _row = 32 * _rb + (_r & 3) + 8 * (_r >> 2) + 4 * hi, _col = 32 * _cb + l31; if (STRICT ? !(_row < _col) : !(_row <= _col)) M[_rb][_cb][_r] = 0.f; } } while (0)
; #define R2_RELANE() do { lane = lt_tid(wvid) & 63; l31 = lane & 31; hi = lane >> 5; } while (0)
; __device__ __forceinline__ void ph_rwkv_chunk(const Params& p, int l, LAS unsigned char* lds, const int wvid) {
;     ...
;             R2_TO_LDS(X, W);
;         }
;         R2_RELANE();
;         {
;             M64 B; R2_ZERO(B); R2_MM_GG(B, BTg, RTg); R2_MASK(B, false); R2_PACK(ABR, B);
	v_mfma_f32_32x32x16_bf16 v[82:97], v[2:5], v[178:181], v[82:97]
	ds_write_b16 v195, v0
	ds_write_b16_d16_hi v195, v0 offset:144
	v_cvt_pk_bf16_f32 v0, v98, v99
	ds_write_b16 v194, v0 offset:64
	ds_write_b16_d16_hi v194, v0 offset:208
	v_cvt_pk_bf16_f32 v0, v100, v101
	ds_write_b16 v224, v0 offset:64
	ds_write_b16_d16_hi v224, v0 offset:208
	v_cvt_pk_bf16_f32 v0, v102, v103
	ds_write_b16 v223, v0 offset:64
	ds_write_b16_d16_hi v223, v0 offset:208
	v_cvt_pk_bf16_f32 v0, v104, v105
	ds_write_b16 v199, v0 offset:64
	ds_write_b16_d16_hi v199, v0 offset:208
	v_cvt_pk_bf16_f32 v0, v106, v107
	ds_write_b16 v198, v0 offset:64
	ds_write_b16_d16_hi v198, v0 offset:208
	v_cvt_pk_bf16_f32 v0, v108, v109
	ds_write_b16 v197, v0 offset:64
	ds_write_b16_d16_hi v197, v0 offset:208
	v_cvt_pk_bf16_f32 v0, v110, v111
	ds_write_b16 v196, v0 offset:64
	ds_write_b16_d16_hi v196, v0 offset:208
	v_cvt_pk_bf16_f32 v0, v112, v113
	v_mfma_f32_32x32x16_bf16 v[66:81], v[2:5], v[150:153], v[66:81]
	ds_write_b16 v195, v0 offset:64
	ds_write_b16_d16_hi v195, v0 offset:208
	v_cvt_pk_bf16_f32 v0, v82, v83
	ds_write_b16 v194, v0 offset:4608
	ds_write_b16_d16_hi v194, v0 offset:4752
	v_cvt_pk_bf16_f32 v0, v84, v85
	ds_write_b16 v193, v0
	ds_write_b16_d16_hi v193, v0 offset:144
	v_cvt_pk_bf16_f32 v0, v86, v87
	ds_write_b16 v193, v0 offset:864
	ds_write_b16_d16_hi v193, v0 offset:1008
	v_cvt_pk_bf16_f32 v0, v88, v89
	ds_write_b16 v193, v0 offset:1152
	ds_write_b16_d16_hi v193, v0 offset:1296
	v_cvt_pk_bf16_f32 v0, v90, v91
	ds_write_b16 v193, v0 offset:2016
	ds_write_b16_d16_hi v193, v0 offset:2160
	v_cvt_pk_bf16_f32 v0, v92, v93
	ds_write_b16 v193, v0 offset:2304
	ds_write_b16_d16_hi v193, v0 offset:2448
	v_cvt_pk_bf16_f32 v0, v94, v95
	ds_write_b16 v193, v0 offset:3168
	ds_write_b16_d16_hi v193, v0 offset:3312
	v_cvt_pk_bf16_f32 v0, v96, v97
	ds_write_b16 v193, v0 offset:3456
	ds_write_b16_d16_hi v193, v0 offset:3600
	v_cvt_pk_bf16_f32 v0, v66, v67
	ds_write_b16 v194, v0 offset:4672
	ds_write_b16_d16_hi v194, v0 offset:4816
	v_cvt_pk_bf16_f32 v0, v68, v69
	ds_write_b16 v193, v0 offset:64
	ds_write_b16_d16_hi v193, v0 offset:208
	v_cvt_pk_bf16_f32 v0, v70, v71
	ds_write_b16 v193, v0 offset:928
	ds_write_b16_d16_hi v193, v0 offset:1072
	v_cvt_pk_bf16_f32 v0, v72, v73
	ds_write_b16 v193, v0 offset:1216
	ds_write_b16_d16_hi v193, v0 offset:1360
	v_cvt_pk_bf16_f32 v0, v74, v75
	ds_write_b16 v193, v0 offset:2080
	ds_write_b16_d16_hi v193, v0 offset:2224
	v_cvt_pk_bf16_f32 v0, v76, v77
	ds_write_b16 v193, v0 offset:2368
	ds_write_b16_d16_hi v193, v0 offset:2512
	v_cvt_pk_bf16_f32 v0, v78, v79
	ds_write_b16 v193, v0 offset:3232
	ds_write_b16_d16_hi v193, v0 offset:3376
	v_cvt_pk_bf16_f32 v0, v80, v81
	ds_write_b16 v193, v0 offset:3520
	ds_write_b16_d16_hi v193, v0 offset:3664
	v_mbcnt_lo_u32_b32 v199, -1, 0
	v_mbcnt_hi_u32_b32 v199, -1, v199
	s_nop 0
	v_and_b32_e32 v119, 31, v199
	v_bfe_u32 v198, v199, 5, 1
	v_lshlrev_b32_e32 v62, 5, v119
	v_lshlrev_b32_e32 v0, 4, v198
	v_or_b32_e32 v114, v0, v62
	v_or_b32_e32 v200, 0x1000, v114
	v_or_b32_e32 v201, 0x1400, v114
	v_or_b32_e32 v202, 0x1800, v114
	v_or_b32_e32 v203, 0x1c00, v114
	global_load_dwordx4 v[72:75], v114, s[70:71]
	global_load_dwordx4 v[76:79], v114, s[54:55]
	global_load_dwordx4 v[80:83], v114, s[54:55] offset:1024
	global_load_dwordx4 v[84:87], v114, s[70:71] offset:1024
	global_load_dwordx4 v[88:91], v114, s[70:71] offset:2048
	global_load_dwordx4 v[92:95], v114, s[54:55] offset:2048
	global_load_dwordx4 v[96:99], v200, s[70:71]
	global_load_dwordx4 v[100:103], v114, s[54:55] offset:3072
	global_load_dwordx4 v[104:107], v114, s[70:71] offset:3072
	global_load_dwordx4 v[108:111], v200, s[54:55]
	global_load_dwordx4 v[132:135], v201, s[70:71]
	global_load_dwordx4 v[136:139], v201, s[54:55]
	global_load_dwordx4 v[140:143], v202, s[70:71]
	global_load_dwordx4 v[144:147], v202, s[54:55]
	global_load_dwordx4 v[232:235], v203, s[70:71]
	global_load_dwordx4 v[236:239], v203, s[54:55]
	s_waitcnt vmcnt(0)
	v_mfma_f32_32x32x16_bf16 v[18:33], v[72:75], v[76:79], 0
	v_or_b32_e32 v117, 0x1000, v114
	v_or_b32_e32 v115, 0x1400, v114
	v_or_b32_e32 v118, 0x1800, v114
	v_or_b32_e32 v116, 0x1c00, v114
	v_lshlrev_b32_e32 v120, 2, v198
	v_cmp_gt_u32_e32 vcc, v120, v119
	s_waitcnt vmcnt(0)
	v_mfma_f32_32x32x16_bf16 v[34:49], v[72:75], v[80:83], 0
	v_cmp_lt_u32_e64 s[0:1], v120, v119
	v_or_b32_e32 v121, 2, v120
	v_lshl_or_b32 v66, v198, 3, v62
	v_or_b32_e32 v122, 3, v120
	s_waitcnt vmcnt(1)
	v_mfma_f32_32x32x16_bf16 v[18:33], v[88:91], v[92:95], v[18:33]
	v_or_b32_e32 v124, 8, v120
	v_or_b32_e32 v123, 9, v120
	v_or_b32_e32 v125, 10, v120
	v_or_b32_e32 v127, 11, v120
	v_or_b32_e32 v126, 16, v120
	v_or_b32_e32 v64, 0x1800, v66
	s_waitcnt vmcnt(0)
	v_mfma_f32_32x32x16_bf16 v[34:49], v[88:91], v[100:103], v[34:49]
	v_or_b32_e32 v128, 17, v120
	v_or_b32_e32 v129, 18, v120
	v_or_b32_e32 v194, 19, v120
	v_or_b32_e32 v193, 24, v120
	v_or_b32_e32 v195, 25, v120
	v_or_b32_e32 v196, 26, v120
	v_mfma_f32_32x32x16_bf16 v[2:17], v[84:87], v[80:83], 0
	v_or_b32_e32 v197, 27, v120
	v_cmp_eq_u32_e64 s[2:3], v121, v119
	v_cmp_eq_u32_e64 s[4:5], v122, v119
	v_cmp_eq_u32_e64 s[6:7], v124, v119
	v_cmp_eq_u32_e64 s[8:9], v123, v119
	v_cmp_eq_u32_e64 s[10:11], v125, v119
	v_cmp_eq_u32_e64 s[16:17], v127, v119
	s_waitcnt vmcnt(0)
	v_mfma_f32_32x32x16_bf16 v[2:17], v[104:107], v[100:103], v[2:17]
	v_cmp_eq_u32_e64 s[18:19], v126, v119
	v_cmp_eq_u32_e64 s[20:21], v128, v119
	v_cmp_eq_u32_e64 s[22:23], v129, v119
	v_cmp_eq_u32_e64 s[24:25], v194, v119
	v_cmp_eq_u32_e64 s[26:27], v193, v119
	s_waitcnt vmcnt(1)
; __device__ __forceinline__ float bflo(unsigned w) { return __uint_as_float(w << 16); }
; __device__ __forceinline__ float bfhi(unsigned w) { return __uint_as_float(w & 0xFFFF0000u); }
; #define R2_ZERO(M) do { _Pragma("unroll") for (int _a = 0; _a < 2; ++_a) _Pragma("unroll") for (int _b = 0; _b < 2; ++_b) _Pragma("unroll") for (int _r = 0; _r < 16; ++_r) M[_a][_b][_r] = 0.f; } while (0)
; #define R2_PACK(Bpk, M) do { _Pragma("unroll") for (int _ks = 0; _ks < 4; ++_ks) _Pragma("unroll") for (int _cb = 0; _cb < 2; ++_cb) Bpk[_ks][_cb] = pack_acc(M[_ks >> 1][_cb], _ks & 1); } while (0)
; #define R2_MASK(M, STRICT) do { _Pragma("unroll") for (int _rb = 0; _rb < 2; ++_rb) _Pragma("unroll") for (int _cb = 0; _cb < 2; ++_cb) _Pragma("unroll") for (int _r = 0; _r < 16; ++_r) { \
;         const int _row = 32 * _rb + (_r & 3) + 8 * (_r >> 2) + 4 * hi, _col = 32 * _cb + l31; if (STRICT ? !(_row < _col) : !(_row <= _col)) M[_rb][_cb][_r] = 0.f; } } while (0)
; __device__ __forceinline__ void ph_rwkv_chunk(const Params& p, int l, LAS unsigned char* lds, const int wvid) {
;     ...
;             M64 B; R2_ZERO(B); R2_MM_GG(B, BTg, RTg); R2_MASK(B, false); R2_PACK(ABR, B);
;         }
;         {
;             M64 G;
; #pragma unroll
;             for (int rb = 0; rb < 2; ++rb)
; #pragma unroll
;                 for (int cb = 0; cb < 2; ++cb)
; #pragma unroll
;                     for (int q = 0; q < 4; ++q) { const u32x2 w = *(const u32x2*)(RTg + TM(32 * cb + l31, 32 * rb + 8 * q + 4 * hi));
;                         G[rb][cb][4 * q] = bflo(w.x); G[rb][cb][4 * q + 1] = bfhi(w.x); G[rb][cb][4 * q + 2] = bflo(w.y); G[rb][cb][4 * q + 3] = bfhi(w.y); }
;             R2_MM_LP(G, X, ABR);
	v_mfma_f32_32x32x16_bf16 v[18:33], v[96:99], v[108:111], v[18:33]
	v_cmp_eq_u32_e64 s[28:29], v195, v119
	v_cmp_eq_u32_e64 s[30:31], v196, v119
	v_cmp_eq_u32_e64 s[34:35], v197, v119
	s_waitcnt vmcnt(0)
	v_mfma_f32_32x32x16_bf16 v[34:49], v[96:99], v[136:139], v[34:49]
	v_mfma_f32_32x32x16_bf16 v[2:17], v[132:135], v[136:139], v[2:17]
	s_waitcnt vmcnt(1)
	v_mfma_f32_32x32x16_bf16 v[18:33], v[140:143], v[144:147], v[18:33]
	s_nop 10
	v_cndmask_b32_e64 v68, 0, v19, s[0:1]
	s_waitcnt vmcnt(0)
	v_mfma_f32_32x32x16_bf16 v[2:17], v[232:235], v[236:239], v[2:17]
	v_cndmask_b32_e64 v54, v18, 0, vcc
	v_cndmask_b32_e64 v67, v54, v18, s[0:1]
	v_cmp_le_u32_e64 s[0:1], v121, v119
	v_or_b32_e32 v18, 0x800, v66
	global_load_dwordx2 v[54:55], v18, s[54:55] offset:16
	v_cndmask_b32_e64 v69, 0, v20, s[0:1]
	v_or_b32_e32 v20, 0x400, v66
	v_cmp_le_u32_e64 s[0:1], v122, v119
	v_mfma_f32_32x32x16_bf16 v[34:49], v[140:143], v[236:239], v[34:49]
	global_load_dwordx2 v[58:59], v66, s[54:55]
	global_load_dwordx2 v[50:51], v66, s[54:55] offset:16
	global_load_dwordx2 v[56:57], v20, s[54:55] offset:16
	global_load_dwordx2 v[52:53], v66, s[54:55] offset:2048
	global_load_dwordx2 v[18:19], v66, s[54:55] offset:1024
	v_cndmask_b32_e64 v70, 0, v21, s[0:1]
	v_cmp_le_u32_e64 s[0:1], v124, v119
	v_or_b32_e32 v20, 0xc00, v66
	global_load_dwordx2 v[60:61], v20, s[54:55] offset:16
	global_load_dwordx2 v[62:63], v66, s[54:55] offset:3072
	v_cndmask_b32_e64 v71, 0, v22, s[0:1]
	v_or_b32_e32 v22, 0x1000, v66
	global_load_dwordx2 v[20:21], v22, s[54:55]
	v_cmp_le_u32_e64 s[0:1], v123, v119
	v_cvt_pk_bf16_f32 v134, v67, v68
	v_cvt_pk_bf16_f32 v135, v69, v70
	v_cndmask_b32_e64 v72, 0, v23, s[0:1]
	v_cmp_le_u32_e64 s[0:1], v125, v119
	v_cvt_pk_bf16_f32 v136, v71, v72
	v_cvt_pk_bf16_f32 v138, v34, v35
	v_cndmask_b32_e64 v73, 0, v24, s[0:1]
	v_cmp_le_u32_e64 s[0:1], v127, v119
	v_cvt_pk_bf16_f32 v139, v36, v37
	v_cvt_pk_bf16_f32 v140, v38, v39
	v_cndmask_b32_e64 v74, 0, v25, s[0:1]
	v_cmp_le_u32_e64 s[0:1], v126, v119
	global_load_dwordx2 v[24:25], v64, s[54:55]
	v_cvt_pk_bf16_f32 v137, v73, v74
	v_cndmask_b32_e64 v130, 0, v26, s[0:1]
	v_or_b32_e32 v26, 0x1400, v66
	global_load_dwordx2 v[100:101], v26, s[54:55]
	global_load_dwordx2 v[104:105], v26, s[54:55] offset:16
	v_cmp_le_u32_e64 s[0:1], v128, v119
	global_load_dwordx2 v[22:23], v22, s[54:55] offset:16
	v_or_b32_e32 v26, 0x1c00, v66
	v_cndmask_b32_e64 v131, 0, v27, s[0:1]
	v_cmp_le_u32_e64 s[0:1], v129, v119
	global_load_dwordx2 v[64:65], v64, s[54:55] offset:16
	v_cvt_pk_bf16_f32 v141, v40, v41
	v_cndmask_b32_e64 v132, 0, v28, s[0:1]
	v_cmp_le_u32_e64 s[0:1], v194, v119
	global_load_dwordx2 v[108:109], v26, s[54:55]
	v_cvt_pk_bf16_f32 v142, v130, v131
	v_cndmask_b32_e64 v133, 0, v29, s[0:1]
	v_cmp_le_u32_e64 s[0:1], v193, v119
	v_cvt_pk_bf16_f32 v143, v132, v133
	v_cvt_pk_bf16_f32 v146, v42, v43
	v_cndmask_b32_e64 v144, 0, v30, s[0:1]
	v_cmp_le_u32_e64 s[0:1], v195, v119
	v_cvt_pk_bf16_f32 v147, v44, v45
	v_cvt_pk_bf16_f32 v148, v46, v47
	v_cndmask_b32_e64 v145, 0, v31, s[0:1]
	global_load_dwordx2 v[30:31], v26, s[54:55] offset:16
	v_cmp_le_u32_e64 s[0:1], v196, v119
	v_cvt_pk_bf16_f32 v144, v144, v145
	v_cvt_pk_bf16_f32 v149, v48, v49
	v_cndmask_b32_e64 v32, 0, v32, s[0:1]
	v_cmp_le_u32_e64 s[0:1], v197, v119
	v_mov_b64_e32 v[132:133], s[42:43]
	v_mov_b64_e32 v[130:131], s[40:41]
	v_or_b32_e32 v34, 48, v120
	v_bfe_u32 v35, v199, 1, 5
	v_mul_u32_u24_e32 v35, 0x90, v35
	s_waitcnt vmcnt(15)
	v_lshlrev_b32_e32 v94, 16, v54
	v_and_b32_e32 v95, 0xffff0000, v54
	v_lshlrev_b32_e32 v96, 16, v55
	v_and_b32_e32 v97, 0xffff0000, v55
	s_waitcnt vmcnt(14)
	v_lshlrev_b32_e32 v82, 16, v58
	s_waitcnt vmcnt(13)
	v_lshlrev_b32_e32 v86, 16, v50
	v_and_b32_e32 v87, 0xffff0000, v50
	v_lshlrev_b32_e32 v88, 16, v51
	s_waitcnt vmcnt(10)
	v_lshlrev_b32_e32 v66, 16, v18
	v_and_b32_e32 v67, 0xffff0000, v18
	v_mul_u32_u24_e32 v18, 0x90, v119
	v_add3_u32 v223, s48, v0, v18
	v_and_b32_e32 v89, 0xffff0000, v51
	v_lshlrev_b32_e32 v90, 16, v52
	v_and_b32_e32 v91, 0xffff0000, v52
	v_lshlrev_b32_e32 v92, 16, v53
	v_and_b32_e32 v93, 0xffff0000, v53
	v_lshlrev_b32_e32 v68, 16, v19
	v_and_b32_e32 v69, 0xffff0000, v19
	s_waitcnt vmcnt(7)
	v_lshlrev_b32_e32 v50, 16, v20
	v_and_b32_e32 v51, 0xffff0000, v20
	v_lshlrev_b32_e32 v52, 16, v21
	v_and_b32_e32 v53, 0xffff0000, v21
	ds_read_b128 v[18:21], v223
	ds_read_b128 v[26:29], v223 offset:4608
	v_and_b32_e32 v83, 0xffff0000, v58
	v_lshlrev_b32_e32 v84, 16, v59
	v_and_b32_e32 v85, 0xffff0000, v59
	v_lshlrev_b32_e32 v70, 16, v56
	v_and_b32_e32 v71, 0xffff0000, v56
	v_lshlrev_b32_e32 v72, 16, v57
	v_and_b32_e32 v73, 0xffff0000, v57
	v_lshlrev_b32_e32 v74, 16, v62
	v_and_b32_e32 v75, 0xffff0000, v62
	v_lshlrev_b32_e32 v76, 16, v63
	v_and_b32_e32 v77, 0xffff0000, v63
	v_lshlrev_b32_e32 v78, 16, v60
	v_and_b32_e32 v79, 0xffff0000, v60
	v_lshlrev_b32_e32 v80, 16, v61
	v_and_b32_e32 v81, 0xffff0000, v61
	s_waitcnt vmcnt(3)
	v_lshlrev_b32_e32 v54, 16, v22
	v_and_b32_e32 v55, 0xffff0000, v22
	v_lshlrev_b32_e32 v56, 16, v23
	v_and_b32_e32 v57, 0xffff0000, v23
	v_lshlrev_b32_e32 v58, 16, v24
	v_and_b32_e32 v59, 0xffff0000, v24
	v_lshlrev_b32_e32 v60, 16, v25
	v_and_b32_e32 v61, 0xffff0000, v25
	ds_read_b128 v[22:25], v223 offset:32
	s_waitcnt lgkmcnt(2)
	v_mfma_f32_32x32x16_bf16 v[82:97], v[18:21], v[134:137], v[82:97]
	s_waitcnt vmcnt(2)
	v_lshlrev_b32_e32 v62, 16, v64
	v_and_b32_e32 v63, 0xffff0000, v64
	v_lshlrev_b32_e32 v64, 16, v65
	v_and_b32_e32 v65, 0xffff0000, v65
	v_lshlrev_b32_e32 v98, 16, v100
	v_and_b32_e32 v99, 0xffff0000, v100
	v_lshlrev_b32_e32 v100, 16, v101
	v_mfma_f32_32x32x16_bf16 v[66:81], v[18:21], v[138:141], v[66:81]
	v_and_b32_e32 v101, 0xffff0000, v101
	v_lshlrev_b32_e32 v102, 16, v104
	v_and_b32_e32 v103, 0xffff0000, v104
	v_lshlrev_b32_e32 v104, 16, v105
	v_and_b32_e32 v105, 0xffff0000, v105
	s_waitcnt vmcnt(1)
; __device__ __forceinline__ float bflo(unsigned w) { return __uint_as_float(w << 16); }
; __device__ __forceinline__ float bfhi(unsigned w) { return __uint_as_float(w & 0xFFFF0000u); }
; __device__ __forceinline__ void ph_rwkv_chunk(const Params& p, int l, LAS unsigned char* lds, const int wvid) {
;     ...
; #pragma unroll
;             for (int rb = 0; rb < 2; ++rb)
; #pragma unroll
;                 for (int cb = 0; cb < 2; ++cb)
; #pragma unroll
;                     for (int q = 0; q < 4; ++q) { const u32x2 w = *(const u32x2*)(RTg + TM(32 * cb + l31, 32 * rb + 8 * q + 4 * hi));
;                         G[rb][cb][4 * q] = bflo(w.x); G[rb][cb][4 * q + 1] = bfhi(w.x); G[rb][cb][4 * q + 2] = bflo(w.y); G[rb][cb][4 * q + 3] = bfhi(w.y); }
;             R2_MM_LP(G, X, ABR);
;             R2_STORE_T(GTg, G, true, 1.0f);
;         }
;         {
;             bf16x8 Bp[4][2]; R2_RAW(Y, BTg); R2_PSEUDO_L(Bp, Y);
	v_lshlrev_b32_e32 v106, 16, v108
	v_and_b32_e32 v107, 0xffff0000, v108
	v_lshlrev_b32_e32 v108, 16, v109
	v_and_b32_e32 v109, 0xffff0000, v109
	s_waitcnt vmcnt(0)
	v_lshlrev_b32_e32 v110, 16, v30
	v_and_b32_e32 v111, 0xffff0000, v30
	v_lshlrev_b32_e32 v112, 16, v31
	v_and_b32_e32 v113, 0xffff0000, v31
	v_cndmask_b32_e64 v0, 0, v33, s[0:1]
	s_waitcnt lgkmcnt(1)
	v_mfma_f32_32x32x16_bf16 v[50:65], v[26:29], v[134:137], v[50:65]
	ds_read_b128 v[18:21], v223 offset:4640
	v_cvt_pk_bf16_f32 v145, v32, v0
	v_or_b32_e32 v0, 32, v119
	s_add_u32 s0, s63, s38
	s_addc_u32 s1, s80, s39
	v_mfma_f32_32x32x16_bf16 v[98:113], v[26:29], v[138:141], v[98:113]
	v_or_b32_e32 v26, 33, v120
	v_or_b32_e32 v27, 34, v120
	v_cndmask_b32_e64 v29, v2, 0, vcc
	v_cmp_le_u32_e32 vcc, v26, v0
	v_or_b32_e32 v28, 43, v120
	s_nop 0
	v_cndmask_b32_e32 v26, 0, v3, vcc
	s_waitcnt lgkmcnt(1)
	v_mfma_f32_32x32x16_bf16 v[82:97], v[22:25], v[142:145], v[82:97]
	v_cmp_le_u32_e32 vcc, v27, v0
	v_cvt_pk_bf16_f32 v170, v29, v26
	s_nop 0
	v_cndmask_b32_e32 v27, 0, v4, vcc
	v_mfma_f32_32x32x16_bf16 v[66:81], v[22:25], v[146:149], v[66:81]
	v_or_b32_e32 v22, 35, v120
	v_cmp_le_u32_e32 vcc, v22, v0
	v_or_b32_e32 v23, 40, v120
	v_or_b32_e32 v24, 41, v120
	v_cndmask_b32_e32 v22, 0, v5, vcc
	ds_read_b128 v[2:5], v223 offset:64
	v_cmp_le_u32_e32 vcc, v23, v0
	v_or_b32_e32 v25, 42, v120
	s_waitcnt lgkmcnt(1)
	v_mfma_f32_32x32x16_bf16 v[50:65], v[18:21], v[142:145], v[50:65]
	v_cndmask_b32_e32 v6, 0, v6, vcc
	v_cmp_le_u32_e32 vcc, v24, v0
	v_cvt_pk_bf16_f32 v171, v27, v22
	v_or_b32_e32 v22, 57, v120
	v_cndmask_b32_e32 v7, 0, v7, vcc
	v_cmp_le_u32_e32 vcc, v25, v0
	v_cvt_pk_bf16_f32 v172, v6, v7
	v_mfma_f32_32x32x16_bf16 v[98:113], v[18:21], v[146:149], v[98:113]
	v_cndmask_b32_e32 v8, 0, v8, vcc
	v_cmp_le_u32_e32 vcc, v28, v0
	v_or_b32_e32 v18, 49, v120
	v_or_b32_e32 v19, 50, v120
	v_cndmask_b32_e32 v9, 0, v9, vcc
	v_cvt_pk_bf16_f32 v173, v8, v9
	v_cmp_le_u32_e32 vcc, v34, v0
	s_waitcnt lgkmcnt(0)
	v_mfma_f32_32x32x16_bf16 v[82:97], v[2:5], v[130:133], v[82:97]
	v_or_b32_e32 v20, 51, v120
	v_cndmask_b32_e32 v10, 0, v10, vcc
	v_cmp_le_u32_e32 vcc, v18, v0
	v_or_b32_e32 v21, 56, v120
	v_or_b32_e32 v23, 58, v120
	v_cndmask_b32_e32 v11, 0, v11, vcc
	v_cmp_le_u32_e32 vcc, v19, v0
	v_mfma_f32_32x32x16_bf16 v[66:81], v[2:5], v[170:173], v[66:81]
	ds_read_b128 v[2:5], v223 offset:4672
	ds_read_b128 v[6:9], v223 offset:96
	v_or_b32_e32 v24, 59, v120
	v_cvt_pk_bf16_f32 v174, v10, v11
	s_waitcnt lgkmcnt(1)
	v_mfma_f32_32x32x16_bf16 v[50:65], v[2:5], v[130:133], v[50:65]
	v_mfma_f32_32x32x16_bf16 v[98:113], v[2:5], v[170:173], v[98:113]
	v_cndmask_b32_e32 v2, 0, v12, vcc
	v_cmp_le_u32_e32 vcc, v20, v0
	s_nop 1
	v_cndmask_b32_e32 v3, 0, v13, vcc
	v_cmp_le_u32_e32 vcc, v21, v0
	v_cvt_pk_bf16_f32 v175, v2, v3
	s_waitcnt lgkmcnt(0)
	v_mfma_f32_32x32x16_bf16 v[82:97], v[6:9], v[130:133], v[82:97]
	v_cndmask_b32_e32 v4, 0, v14, vcc
	v_cmp_le_u32_e32 vcc, v22, v0
	s_nop 1
	v_cndmask_b32_e32 v5, 0, v15, vcc
	v_cvt_pk_bf16_f32 v176, v4, v5
	ds_read_b128 v[2:5], v223 offset:4704
	v_cmp_le_u32_e32 vcc, v23, v0
	s_waitcnt lgkmcnt(0)
	v_mfma_f32_32x32x16_bf16 v[50:65], v[2:5], v[130:133], v[50:65]
	v_cndmask_b32_e32 v12, 0, v16, vcc
	v_cmp_le_u32_e32 vcc, v24, v0
	s_nop 1
	v_cndmask_b32_e32 v0, 0, v17, vcc
	v_cvt_pk_bf16_f32 v177, v12, v0
	v_and_b32_e32 v0, 63, v199
	v_lshlrev_b32_e32 v0, 4, v0
	v_mfma_f32_32x32x16_bf16 v[66:81], v[6:9], v[174:177], v[66:81]
	v_lshl_add_u64 v[18:19], s[70:71], 0, v[0:1]
	v_add_co_u32_e32 v30, vcc, s44, v18
	s_nop 1
	v_addc_co_u32_e32 v31, vcc, 0, v19, vcc
	v_cmp_eq_u32_e32 vcc, v120, v119
	v_mfma_f32_32x32x16_bf16 v[98:113], v[2:5], v[174:177], v[98:113]
	v_cvt_pk_bf16_f32 v2, v82, v83
	v_cvt_pk_bf16_f32 v3, v84, v85
	v_cvt_pk_bf16_f32 v4, v86, v87
	v_cvt_pk_bf16_f32 v5, v88, v89
	global_store_dwordx4 v114, v[2:5], s[0:1]
	s_nop 1
	v_cvt_pk_bf16_f32 v2, v90, v91
	v_cvt_pk_bf16_f32 v3, v92, v93
	v_cvt_pk_bf16_f32 v4, v94, v95
	v_cvt_pk_bf16_f32 v5, v96, v97
	global_store_dwordx4 v114, v[2:5], s[0:1] offset:2048
	s_nop 1
	v_cvt_pk_bf16_f32 v2, v66, v67
	v_cvt_pk_bf16_f32 v3, v68, v69
	v_cvt_pk_bf16_f32 v4, v70, v71
	v_cvt_pk_bf16_f32 v5, v72, v73
	global_store_dwordx4 v114, v[2:5], s[0:1] offset:1024
	s_nop 1
	v_cvt_pk_bf16_f32 v2, v74, v75
	v_cvt_pk_bf16_f32 v3, v76, v77
	v_cvt_pk_bf16_f32 v4, v78, v79
	v_cvt_pk_bf16_f32 v5, v80, v81
	global_store_dwordx4 v114, v[2:5], s[0:1] offset:3072
	s_nop 1
	v_cvt_pk_bf16_f32 v2, v50, v51
	v_cvt_pk_bf16_f32 v3, v52, v53
	v_cvt_pk_bf16_f32 v4, v54, v55
	v_cvt_pk_bf16_f32 v5, v56, v57
	global_store_dwordx4 v117, v[2:5], s[0:1]
	s_nop 1
	v_cvt_pk_bf16_f32 v2, v58, v59
	v_cvt_pk_bf16_f32 v3, v60, v61
	v_cvt_pk_bf16_f32 v4, v62, v63
	v_cvt_pk_bf16_f32 v5, v64, v65
	global_store_dwordx4 v118, v[2:5], s[0:1]
	s_nop 1
	v_cvt_pk_bf16_f32 v2, v98, v99
	v_cvt_pk_bf16_f32 v3, v100, v101
	v_cvt_pk_bf16_f32 v4, v102, v103
	v_cvt_pk_bf16_f32 v5, v104, v105
	global_store_dwordx4 v115, v[2:5], s[0:1]
	s_nop 1
	v_cvt_pk_bf16_f32 v2, v106, v107
	v_cvt_pk_bf16_f32 v3, v108, v109
	v_cvt_pk_bf16_f32 v4, v110, v111
	v_cvt_pk_bf16_f32 v5, v112, v113
	global_store_dwordx4 v116, v[2:5], s[0:1]
	global_load_dwordx4 v[2:5], v0, s[70:71]
	s_nop 0
	global_load_dwordx4 v[6:9], v0, s[70:71] offset:1024
	global_load_dwordx4 v[10:13], v0, s[70:71] offset:2048
	global_load_dwordx4 v[14:17], v0, s[70:71] offset:3072
	global_load_dwordx4 v[18:21], v[30:31], off
	global_load_dwordx4 v[22:25], v[30:31], off offset:1024
	global_load_dwordx4 v[26:29], v[30:31], off offset:2048
	s_nop 0
	global_load_dwordx4 v[30:33], v[30:31], off offset:3072
	v_lshlrev_b32_e32 v0, 4, v199
	v_and_b32_e32 v0, 16, v0
	v_add3_u32 v0, s48, v35, v0
	s_waitcnt vmcnt(7)
; #define R2_ZERO(M) do { _Pragma("unroll") for (int _a = 0; _a < 2; ++_a) _Pragma("unroll") for (int _b = 0; _b < 2; ++_b) _Pragma("unroll") for (int _r = 0; _r < 16; ++_r) M[_a][_b][_r] = 0.f; } while (0)
; __device__ __forceinline__ void ph_rwkv_chunk(const Params& p, int l, LAS unsigned char* lds, const int wvid) {
;     ...
;             bf16x8 Bp[4][2]; R2_RAW(Y, BTg); R2_PSEUDO_L(Bp, Y);
;             M64 P; R2_ZERO(P); R2_MM_LP(P, X, Bp);
; #pragma unroll
;             for (int rb = 0; rb < 2; ++rb)
; #pragma unroll
;                 for (int r = 0; r < 16; ++r) if (((r & 3) + 8 * (r >> 2) + 4 * hi) == l31) P[rb][rb][r] += 1.f;
	ds_write_b128 v0, v[2:5] offset:9216
	s_waitcnt vmcnt(6)
	ds_write_b128 v0, v[6:9] offset:13824
	s_waitcnt vmcnt(5)
	ds_write_b128 v0, v[10:13] offset:9248
	s_waitcnt vmcnt(4)
	ds_write_b128 v0, v[14:17] offset:13856
	s_waitcnt vmcnt(3)
	ds_write_b128 v0, v[18:21] offset:9280
	s_waitcnt vmcnt(2)
	ds_write_b128 v0, v[22:25] offset:13888
	s_waitcnt vmcnt(1)
	ds_write_b128 v0, v[26:29] offset:9312
	s_waitcnt vmcnt(0)
	ds_write_b128 v0, v[30:33] offset:13920
	v_lshlrev_b32_e32 v0, 1, v119
	v_mul_u32_u24_e32 v2, 0x240, v198
	v_mul_u32_u24_e32 v3, 0x90, v121
	v_mul_u32_u24_e32 v4, 0x90, v34
	v_add3_u32 v2, s48, v2, v0
	v_add3_u32 v3, s48, v3, v0
	v_add3_u32 v0, s48, v4, v0
	ds_read_u16 v6, v2 offset:9216
	ds_read_u16 v7, v2 offset:9360
	ds_read_u16 v9, v2 offset:10656
	ds_read_u16 v10, v2 offset:10800
	ds_read_u16 v11, v2 offset:10864
	ds_read_u16 v12, v2 offset:10720
	ds_read_u16 v13, v2 offset:9424
	ds_read_u16 v14, v2 offset:9280
	ds_read_u16 v8, v3 offset:9216
	ds_read_u16 v15, v3 offset:9360
	ds_read_u16 v16, v3 offset:10080
	ds_read_u16 v17, v3 offset:10224
	ds_read_u16 v18, v3 offset:10288
	ds_read_u16 v19, v3 offset:10144
	ds_read_u16 v20, v3 offset:9424
	ds_read_u16 v21, v3 offset:9280
	ds_read_u16 v70, v3 offset:11232
	ds_read_u16 v71, v3 offset:11376
	ds_read_u16 v74, v3 offset:11440
	ds_read_u16 v78, v0 offset:9216
	ds_read_u16 v79, v0 offset:9360
	ds_read_u16 v80, v0 offset:9424
	ds_read_u16 v0, v0 offset:9280
	ds_read_u16 v75, v3 offset:11296
	ds_read_u16 v72, v2 offset:11808
	ds_read_u16 v73, v2 offset:11952
	ds_read_u16 v76, v2 offset:12672
	ds_read_u16 v77, v2 offset:12816
	ds_read_u16 v81, v2 offset:12880
	ds_read_u16 v82, v2 offset:12736
	ds_read_u16 v83, v2 offset:12016
	ds_read_u16 v84, v2 offset:11872
	ds_read_u16 v85, v2 offset:12960
	ds_read_u16 v86, v2 offset:13104
	ds_read_u16 v87, v2 offset:13168
	ds_read_u16 v88, v2 offset:13824
	ds_read_u16 v89, v2 offset:13968
	ds_read_u16 v90, v2 offset:14032
	ds_read_u16 v91, v2 offset:13888
	ds_read_u16 v92, v2 offset:13024
	ds_read_u16 v93, v2 offset:14112
	ds_read_u16 v94, v2 offset:14256
	ds_read_u16 v95, v2 offset:14976
	ds_read_u16 v96, v2 offset:15120
	ds_read_u16 v97, v2 offset:15184
	ds_read_u16 v98, v2 offset:15040
	ds_read_u16 v99, v2 offset:14320
	ds_read_u16 v100, v2 offset:14176
	ds_read_u16 v101, v2 offset:15264
	ds_read_u16 v102, v2 offset:15408
	ds_read_u16 v103, v2 offset:15472
	ds_read_u16 v104, v2 offset:16416
	ds_read_u16 v105, v2 offset:16560
	ds_read_u16 v106, v2 offset:16624
	ds_read_u16 v107, v2 offset:16480
	ds_read_u16 v108, v2 offset:15328
	ds_read_u16 v109, v2 offset:17280
	ds_read_u16 v110, v2 offset:17424
	ds_read_u16 v111, v2 offset:17568
	ds_read_u16 v112, v2 offset:17712
	ds_read_u16 v113, v2 offset:17776
	ds_read_u16 v198, v2 offset:17632
	ds_read_u16 v199, v2 offset:17488
	ds_read_u16 v200, v2 offset:17344
	ds_read_b128 v[2:5], v223
	ds_read_b128 v[66:69], v223 offset:32
	s_waitcnt lgkmcnt(14)
	v_lshl_or_b32 v6, v7, 16, v6
	v_lshl_or_b32 v7, v15, 16, v8
	v_lshl_or_b32 v8, v17, 16, v16
	v_lshl_or_b32 v9, v10, 16, v9
	v_lshl_or_b32 v34, v13, 16, v14
	v_lshl_or_b32 v35, v20, 16, v21
	v_lshl_or_b32 v36, v18, 16, v19
	v_lshl_or_b32 v37, v11, 16, v12
	s_waitcnt lgkmcnt(1)
	v_mfma_f32_32x32x16_bf16 v[50:65], v[2:5], v[6:9], 0
	ds_read_b128 v[38:41], v223 offset:4608
	v_lshl_or_b32 v70, v71, 16, v70
	v_lshl_or_b32 v71, v73, 16, v72
	v_lshl_or_b32 v72, v77, 16, v76
	v_lshl_or_b32 v73, v86, 16, v85
	v_lshl_or_b32 v74, v74, 16, v75
	v_lshl_or_b32 v75, v83, 16, v84
	v_mfma_f32_32x32x16_bf16 v[18:33], v[2:5], v[34:37], 0
	v_lshl_or_b32 v76, v81, 16, v82
	v_lshl_or_b32 v77, v87, 16, v92
	s_waitcnt lgkmcnt(1)
	v_mfma_f32_32x32x16_bf16 v[50:65], v[66:69], v[70:73], v[50:65]
	v_mfma_f32_32x32x16_bf16 v[18:33], v[66:69], v[74:77], v[18:33]
	ds_read_b128 v[66:69], v223 offset:4640
	s_waitcnt lgkmcnt(1)
	v_mfma_f32_32x32x16_bf16 v[2:17], v[38:41], v[6:9], 0
	v_mfma_f32_32x32x16_bf16 v[34:49], v[38:41], v[34:37], 0
	s_waitcnt lgkmcnt(0)
	v_mfma_f32_32x32x16_bf16 v[2:17], v[66:69], v[70:73], v[2:17]
	v_lshl_or_b32 v70, v89, 16, v88
	v_lshl_or_b32 v71, v94, 16, v93
	v_lshl_or_b32 v72, v96, 16, v95
	v_lshl_or_b32 v73, v102, 16, v101
	v_mfma_f32_32x32x16_bf16 v[34:49], v[66:69], v[74:77], v[34:49]
	ds_read_b128 v[66:69], v223 offset:64
	v_lshl_or_b32 v74, v90, 16, v91
	v_lshl_or_b32 v75, v99, 16, v100
	v_lshl_or_b32 v76, v97, 16, v98
	v_lshl_or_b32 v77, v103, 16, v108
	s_waitcnt lgkmcnt(0)
	v_mfma_f32_32x32x16_bf16 v[50:65], v[66:69], v[70:73], v[50:65]
	v_mfma_f32_32x32x16_bf16 v[18:33], v[66:69], v[74:77], v[18:33]
	ds_read_b128 v[66:69], v223 offset:4672
	s_waitcnt lgkmcnt(0)
	v_mfma_f32_32x32x16_bf16 v[2:17], v[66:69], v[70:73], v[2:17]
	v_lshl_or_b32 v70, v79, 16, v78
	v_lshl_or_b32 v71, v105, 16, v104
	v_lshl_or_b32 v72, v110, 16, v109
	v_lshl_or_b32 v73, v112, 16, v111
	v_mfma_f32_32x32x16_bf16 v[34:49], v[66:69], v[74:77], v[34:49]
	ds_read_b128 v[66:69], v223 offset:96
	v_lshl_or_b32 v74, v80, 16, v0
	v_lshl_or_b32 v75, v106, 16, v107
	v_lshl_or_b32 v76, v199, 16, v200
	v_lshl_or_b32 v77, v113, 16, v198
	v_or_b32_e32 v0, 1, v120
	v_cmp_eq_u32_e64 s[0:1], v0, v119
	s_waitcnt lgkmcnt(0)
	v_mfma_f32_32x32x16_bf16 v[50:65], v[66:69], v[70:73], v[50:65]
	v_mfma_f32_32x32x16_bf16 v[18:33], v[66:69], v[74:77], v[18:33]
	ds_read_b128 v[66:69], v223 offset:4704
	s_nop 9
	v_add_f32_e32 v0, 1.0, v52
	v_cndmask_b32_e64 v52, v52, v0, s[2:3]
	v_add_f32_e32 v0, 1.0, v53
	v_cndmask_b32_e64 v53, v53, v0, s[4:5]
	v_add_f32_e32 v0, 1.0, v54
	v_cndmask_b32_e64 v54, v54, v0, s[6:7]
	v_add_f32_e32 v0, 1.0, v55
	v_cndmask_b32_e64 v55, v55, v0, s[8:9]
	v_add_f32_e32 v0, 1.0, v56
	v_cndmask_b32_e64 v56, v56, v0, s[10:11]
	v_add_f32_e32 v0, 1.0, v57
	s_waitcnt lgkmcnt(0)
; #define R2_ZERO(M) do { _Pragma("unroll") for (int _a = 0; _a < 2; ++_a) _Pragma("unroll") for (int _b = 0; _b < 2; ++_b) _Pragma("unroll") for (int _r = 0; _r < 16; ++_r) M[_a][_b][_r] = 0.f; } while (0)
; #define R2_MASK(M, STRICT) do { _Pragma("unroll") for (int _rb = 0; _rb < 2; ++_rb) _Pragma("unroll") for (int _cb = 0; _cb < 2; ++_cb) _Pragma("unroll") for (int _r = 0; _r < 16; ++_r) { \
;         const int _row = 32 * _rb + (_r & 3) + 8 * (_r >> 2) + 4 * hi, _col = 32 * _cb + l31; if (STRICT ? !(_row < _col) : !(_row <= _col)) M[_rb][_cb][_r] = 0.f; } } while (0)
; #define R2_RELANE() do { lane = lt_tid(wvid) & 63; l31 = lane & 31; hi = lane >> 5; } while (0)
; __device__ __forceinline__ void ph_rwkv_chunk(const Params& p, int l, LAS unsigned char* lds, const int wvid) {
;     ...
;             M64 P; R2_ZERO(P); R2_MM_LP(P, X, Bp);
; #pragma unroll
;             for (int rb = 0; rb < 2; ++rb)
; #pragma unroll
;                 for (int r = 0; r < 16; ++r) if (((r & 3) + 8 * (r >> 2) + 4 * hi) == l31) P[rb][rb][r] += 1.f;
; #pragma unroll
;             for (int rb = 0; rb < 2; ++rb)
; #pragma unroll
;                 for (int r = 0; r < 16; ++r) { P[rb][0][r] *= gc0; P[rb][1][r] *= gc1; }
;             R2_STORE_T(PTg, P, true, 1.0f);
;         }
;         R2_RELANE();
;         bf16x8 Zpk[4][2];
;         {
;             M64 A; R2_ZERO(A); R2_MM_GG(A, KTg, ATg); R2_MASK(A, true);
	v_mfma_f32_32x32x16_bf16 v[34:49], v[66:69], v[74:77], v[34:49]
	v_cndmask_b32_e64 v57, v57, v0, s[16:17]
	v_add_f32_e32 v0, 1.0, v58
	v_cndmask_b32_e64 v58, v58, v0, s[18:19]
	v_add_f32_e32 v0, 1.0, v59
	v_cndmask_b32_e64 v59, v59, v0, s[20:21]
	v_add_f32_e32 v0, 1.0, v60
	v_cndmask_b32_e64 v60, v60, v0, s[22:23]
	v_add_f32_e32 v0, 1.0, v61
	v_cndmask_b32_e64 v61, v61, v0, s[24:25]
	v_add_f32_e32 v0, 1.0, v62
	v_cndmask_b32_e64 v62, v62, v0, s[26:27]
	v_add_f32_e32 v0, 1.0, v63
	v_cndmask_b32_e64 v63, v63, v0, s[28:29]
	v_add_f32_e32 v0, 1.0, v64
	v_cndmask_b32_e64 v64, v64, v0, s[30:31]
	v_add_f32_e32 v0, 1.0, v65
	v_cndmask_b32_e64 v65, v65, v0, s[34:35]
	v_add_f32_e32 v0, 1.0, v34
	v_cndmask_b32_e32 v34, v34, v0, vcc
	v_add_f32_e32 v0, 1.0, v35
	v_cndmask_b32_e64 v35, v35, v0, s[0:1]
	v_add_f32_e32 v0, 1.0, v36
	v_mfma_f32_32x32x16_bf16 v[2:17], v[66:69], v[70:73], v[2:17]
	v_cndmask_b32_e64 v36, v36, v0, s[2:3]
	v_add_f32_e32 v0, 1.0, v37
	v_cndmask_b32_e64 v37, v37, v0, s[4:5]
	v_add_f32_e32 v0, 1.0, v38
	v_cndmask_b32_e64 v38, v38, v0, s[6:7]
	v_add_f32_e32 v0, 1.0, v39
	v_cndmask_b32_e64 v39, v39, v0, s[8:9]
	v_add_f32_e32 v0, 1.0, v40
	v_add_f32_e32 v66, 1.0, v50
	v_cndmask_b32_e64 v40, v40, v0, s[10:11]
	v_add_f32_e32 v0, 1.0, v41
	v_cndmask_b32_e32 v50, v50, v66, vcc
	v_add_f32_e32 v66, 1.0, v51
	v_cndmask_b32_e64 v41, v41, v0, s[16:17]
	v_add_f32_e32 v0, 1.0, v42
	v_cndmask_b32_e64 v51, v51, v66, s[0:1]
	v_cndmask_b32_e64 v42, v42, v0, s[18:19]
	v_add_f32_e32 v0, 1.0, v43
	v_cndmask_b32_e64 v43, v43, v0, s[20:21]
	v_add_f32_e32 v0, 1.0, v44
	v_pk_mul_f32 v[50:51], v[192:193], v[50:51] op_sel_hi:[0,1]
	v_pk_mul_f32 v[52:53], v[192:193], v[52:53] op_sel_hi:[0,1]
	v_pk_mul_f32 v[54:55], v[192:193], v[54:55] op_sel_hi:[0,1]
	v_pk_mul_f32 v[56:57], v[192:193], v[56:57] op_sel_hi:[0,1]
	v_cndmask_b32_e64 v44, v44, v0, s[22:23]
	v_add_f32_e32 v0, 1.0, v45
	v_pk_mul_f32 v[58:59], v[192:193], v[58:59] op_sel_hi:[0,1]
	v_pk_mul_f32 v[60:61], v[192:193], v[60:61] op_sel_hi:[0,1]
	v_pk_mul_f32 v[62:63], v[192:193], v[62:63] op_sel_hi:[0,1]
	v_pk_mul_f32 v[64:65], v[192:193], v[64:65] op_sel_hi:[0,1]
	v_pk_mul_f32 v[66:67], v[192:193], v[2:3] op_sel_hi:[0,1]
	v_pk_mul_f32 v[68:69], v[192:193], v[4:5] op_sel_hi:[0,1]
	v_cvt_pk_bf16_f32 v2, v50, v51
	v_cvt_pk_bf16_f32 v3, v52, v53
	v_cvt_pk_bf16_f32 v4, v54, v55
	v_cvt_pk_bf16_f32 v5, v56, v57
	v_cndmask_b32_e64 v45, v45, v0, s[24:25]
	v_add_f32_e32 v0, 1.0, v46
	v_pk_mul_f32 v[18:19], v[190:191], v[18:19] op_sel_hi:[0,1]
	v_pk_mul_f32 v[20:21], v[190:191], v[20:21] op_sel_hi:[0,1]
	v_pk_mul_f32 v[22:23], v[190:191], v[22:23] op_sel_hi:[0,1]
	v_pk_mul_f32 v[24:25], v[190:191], v[24:25] op_sel_hi:[0,1]
	global_store_dwordx4 v114, v[2:5], s[72:73]
	v_cndmask_b32_e64 v46, v46, v0, s[26:27]
	v_add_f32_e32 v0, 1.0, v47
	v_cvt_pk_bf16_f32 v2, v58, v59
	v_cvt_pk_bf16_f32 v3, v60, v61
	v_cvt_pk_bf16_f32 v4, v62, v63
	v_cvt_pk_bf16_f32 v5, v64, v65
	v_pk_mul_f32 v[26:27], v[190:191], v[26:27] op_sel_hi:[0,1]
	v_pk_mul_f32 v[28:29], v[190:191], v[28:29] op_sel_hi:[0,1]
	v_pk_mul_f32 v[30:31], v[190:191], v[30:31] op_sel_hi:[0,1]
	v_pk_mul_f32 v[32:33], v[190:191], v[32:33] op_sel_hi:[0,1]
	global_store_dwordx4 v114, v[2:5], s[72:73] offset:2048
	v_cndmask_b32_e64 v47, v47, v0, s[28:29]
	v_add_f32_e32 v0, 1.0, v48
	v_cvt_pk_bf16_f32 v2, v18, v19
	v_cvt_pk_bf16_f32 v3, v20, v21
	v_cvt_pk_bf16_f32 v4, v22, v23
	v_cvt_pk_bf16_f32 v5, v24, v25
	v_pk_mul_f32 v[6:7], v[192:193], v[6:7] op_sel_hi:[0,1]
	v_pk_mul_f32 v[8:9], v[192:193], v[8:9] op_sel_hi:[0,1]
	global_store_dwordx4 v114, v[2:5], s[72:73] offset:1024
	v_cndmask_b32_e64 v48, v48, v0, s[30:31]
	v_add_f32_e32 v0, 1.0, v49
	v_cvt_pk_bf16_f32 v2, v26, v27
	v_cvt_pk_bf16_f32 v3, v28, v29
	v_cvt_pk_bf16_f32 v4, v30, v31
	v_cvt_pk_bf16_f32 v5, v32, v33
	v_pk_mul_f32 v[10:11], v[192:193], v[10:11] op_sel_hi:[0,1]
	v_pk_mul_f32 v[12:13], v[192:193], v[12:13] op_sel_hi:[0,1]
	v_pk_mul_f32 v[14:15], v[192:193], v[14:15] op_sel_hi:[0,1]
	v_pk_mul_f32 v[16:17], v[192:193], v[16:17] op_sel_hi:[0,1]
	global_store_dwordx4 v114, v[2:5], s[72:73] offset:3072
	v_cndmask_b32_e64 v49, v49, v0, s[34:35]
	v_pk_mul_f32 v[34:35], v[190:191], v[34:35] op_sel_hi:[0,1]
	v_cvt_pk_bf16_f32 v2, v66, v67
	v_cvt_pk_bf16_f32 v3, v68, v69
	v_cvt_pk_bf16_f32 v4, v6, v7
	v_cvt_pk_bf16_f32 v5, v8, v9
	v_pk_mul_f32 v[36:37], v[190:191], v[36:37] op_sel_hi:[0,1]
	v_pk_mul_f32 v[38:39], v[190:191], v[38:39] op_sel_hi:[0,1]
	v_pk_mul_f32 v[40:41], v[190:191], v[40:41] op_sel_hi:[0,1]
	global_store_dwordx4 v117, v[2:5], s[72:73]
	v_pk_mul_f32 v[42:43], v[190:191], v[42:43] op_sel_hi:[0,1]
	v_pk_mul_f32 v[44:45], v[190:191], v[44:45] op_sel_hi:[0,1]
	v_cvt_pk_bf16_f32 v2, v10, v11
	v_cvt_pk_bf16_f32 v3, v12, v13
	v_cvt_pk_bf16_f32 v4, v14, v15
	v_cvt_pk_bf16_f32 v5, v16, v17
	v_pk_mul_f32 v[46:47], v[190:191], v[46:47] op_sel_hi:[0,1]
	v_pk_mul_f32 v[48:49], v[190:191], v[48:49] op_sel_hi:[0,1]
	global_store_dwordx4 v118, v[2:5], s[72:73]
	s_add_u32 s34, s93, s38
	s_addc_u32 s35, s62, s39
	v_cvt_pk_bf16_f32 v2, v34, v35
	v_cvt_pk_bf16_f32 v3, v36, v37
	v_cvt_pk_bf16_f32 v4, v38, v39
	v_cvt_pk_bf16_f32 v5, v40, v41
	global_store_dwordx4 v115, v[2:5], s[72:73]
	s_add_u32 s42, s95, s38
	s_addc_u32 s43, s51, s39
	v_cvt_pk_bf16_f32 v2, v42, v43
	v_cvt_pk_bf16_f32 v3, v44, v45
	v_cvt_pk_bf16_f32 v4, v46, v47
	v_cvt_pk_bf16_f32 v5, v48, v49
	global_store_dwordx4 v116, v[2:5], s[72:73]
	v_mbcnt_lo_u32_b32 v66, -1, 0
	v_mbcnt_hi_u32_b32 v66, -1, v66
	s_nop 0
	v_bfe_u32 v62, v66, 5, 1
	v_and_b32_e32 v0, 31, v66
	v_lshlrev_b32_e32 v63, 4, v62
	v_lshl_or_b32 v64, v0, 5, v63
	v_or_b32_e32 v196, 0x1000, v64
	v_or_b32_e32 v197, 0x1400, v64
	v_or_b32_e32 v198, 0x1800, v64
	v_or_b32_e32 v199, 0x1c00, v64
	global_load_dwordx4 v[68:71], v64, s[36:37]
	global_load_dwordx4 v[72:75], v64, s[86:87]
	global_load_dwordx4 v[76:79], v64, s[86:87] offset:1024
	global_load_dwordx4 v[80:83], v64, s[36:37] offset:1024
	global_load_dwordx4 v[84:87], v64, s[36:37] offset:2048
	global_load_dwordx4 v[88:91], v64, s[86:87] offset:2048
	global_load_dwordx4 v[92:95], v196, s[36:37]
	global_load_dwordx4 v[96:99], v64, s[86:87] offset:3072
	global_load_dwordx4 v[100:103], v64, s[36:37] offset:3072
	global_load_dwordx4 v[104:107], v196, s[86:87]
	global_load_dwordx4 v[108:111], v197, s[86:87]
	global_load_dwordx4 v[112:115], v197, s[36:37]
	global_load_dwordx4 v[116:119], v198, s[36:37]
	global_load_dwordx4 v[120:123], v198, s[86:87]
	global_load_dwordx4 v[124:127], v199, s[86:87]
	global_load_dwordx4 v[232:235], v199, s[36:37]
	s_waitcnt vmcnt(4)
; #define R2_ZERO(M) do { _Pragma("unroll") for (int _a = 0; _a < 2; ++_a) _Pragma("unroll") for (int _b = 0; _b < 2; ++_b) _Pragma("unroll") for (int _r = 0; _r < 16; ++_r) M[_a][_b][_r] = 0.f; } while (0)
; #define R2_MASK(M, STRICT) do { _Pragma("unroll") for (int _rb = 0; _rb < 2; ++_rb) _Pragma("unroll") for (int _cb = 0; _cb < 2; ++_cb) _Pragma("unroll") for (int _r = 0; _r < 16; ++_r) { \
;         const int _row = 32 * _rb + (_r & 3) + 8 * (_r >> 2) + 4 * hi, _col = 32 * _cb + l31; if (STRICT ? !(_row < _col) : !(_row <= _col)) M[_rb][_cb][_r] = 0.f; } } while (0)
; __device__ __forceinline__ void ph_rwkv_chunk(const Params& p, int l, LAS unsigned char* lds, const int wvid) {
;     ...
;             M64 A; R2_ZERO(A); R2_MM_GG(A, KTg, ATg); R2_MASK(A, true);
;             asm volatile("" ::: "memory");
;             R2_TO_LDS(X, A);
	v_mfma_f32_32x32x16_bf16 v[34:49], v[68:71], v[72:75], 0
	v_or_b32_e32 v65, 0x1000, v64
	s_waitcnt vmcnt(1)
	v_mfma_f32_32x32x16_bf16 v[34:49], v[84:87], v[88:91], v[34:49]
	v_mfma_f32_32x32x16_bf16 v[2:17], v[68:71], v[76:79], 0
	s_waitcnt vmcnt(0)
	v_mfma_f32_32x32x16_bf16 v[2:17], v[84:87], v[96:99], v[2:17]
	v_mfma_f32_32x32x16_bf16 v[18:33], v[80:83], v[76:79], 0
	s_waitcnt vmcnt(0)
	v_mfma_f32_32x32x16_bf16 v[18:33], v[100:103], v[96:99], v[18:33]
	v_or_b32_e32 v54, 0x1400, v64
	v_or_b32_e32 v65, 0x1800, v64
	s_waitcnt vmcnt(0)
	v_mfma_f32_32x32x16_bf16 v[34:49], v[92:95], v[104:107], v[34:49]
	s_nop 0
	s_waitcnt vmcnt(1)
	v_mfma_f32_32x32x16_bf16 v[2:17], v[92:95], v[108:111], v[2:17]
	s_waitcnt vmcnt(1)
	v_mfma_f32_32x32x16_bf16 v[18:33], v[112:115], v[108:111], v[18:33]
	v_or_b32_e32 v54, 0x1c00, v64
	s_waitcnt vmcnt(0)
	v_mfma_f32_32x32x16_bf16 v[34:49], v[116:119], v[120:123], v[34:49]
	s_nop 0
	s_waitcnt vmcnt(1)
	v_mfma_f32_32x32x16_bf16 v[2:17], v[116:119], v[124:127], v[2:17]
	s_nop 11
	v_cvt_pk_bf16_f32 v2, v2, v3
	s_waitcnt vmcnt(0)
	v_mfma_f32_32x32x16_bf16 v[18:33], v[232:235], v[124:127], v[18:33]
	v_lshlrev_b32_e32 v50, 2, v62
	v_or_b32_e32 v52, 3, v50
	v_cmp_lt_u32_e64 s[2:3], v52, v0
	v_or_b32_e32 v52, 8, v50
	v_cmp_lt_u32_e64 s[4:5], v52, v0
	v_or_b32_e32 v52, 9, v50
	v_cmp_lt_u32_e64 s[6:7], v52, v0
	v_or_b32_e32 v52, 10, v50
	v_cmp_lt_u32_e64 s[8:9], v52, v0
	v_or_b32_e32 v52, 11, v50
	v_cmp_lt_u32_e64 s[10:11], v52, v0
	v_or_b32_e32 v52, 16, v50
	v_cmp_lt_u32_e64 s[16:17], v52, v0
	v_or_b32_e32 v52, 17, v50
	v_cmp_lt_u32_e64 s[18:19], v52, v0
	v_or_b32_e32 v52, 18, v50
	v_cmp_lt_u32_e64 s[20:21], v52, v0
	v_or_b32_e32 v52, 19, v50
	v_cmp_lt_u32_e64 s[22:23], v52, v0
	v_or_b32_e32 v52, 24, v50
	v_cmp_lt_u32_e64 s[24:25], v52, v0
	v_or_b32_e32 v52, 25, v50
	v_cmp_lt_u32_e64 s[26:27], v52, v0
	v_or_b32_e32 v52, 26, v50
	v_cmp_lt_u32_e64 s[28:29], v52, v0
	v_or_b32_e32 v52, 27, v50
	v_cmp_lt_u32_e64 s[30:31], v52, v0
	s_or_b64 s[28:29], s[30:31], s[28:29]
	s_or_b64 s[26:27], s[28:29], s[26:27]
	s_or_b64 s[24:25], s[26:27], s[24:25]
	s_or_b64 s[22:23], s[24:25], s[22:23]
	s_or_b64 s[20:21], s[22:23], s[20:21]
	s_or_b64 s[18:19], s[20:21], s[18:19]
	s_or_b64 s[16:17], s[18:19], s[16:17]
	s_or_b64 s[10:11], s[16:17], s[10:11]
	s_or_b64 s[8:9], s[10:11], s[8:9]
	v_or_b32_e32 v51, 1, v50
	s_or_b64 s[6:7], s[8:9], s[6:7]
	v_cmp_lt_u32_e32 vcc, v51, v0
	v_or_b32_e32 v51, 2, v50
	s_or_b64 s[4:5], s[6:7], s[4:5]
	v_cmp_lt_u32_e64 s[0:1], v51, v0
	s_or_b64 s[2:3], s[4:5], s[2:3]
	s_or_b64 s[0:1], s[2:3], s[0:1]
	v_cndmask_b32_e64 v36, 0, v36, s[0:1]
	s_or_b64 vcc, s[0:1], vcc
	v_cmp_lt_u32_e64 s[0:1], v50, v0
	v_or_b32_e32 v52, 32, v0
	v_or_b32_e32 v53, 33, v50
	v_or_b32_e32 v54, 34, v50
	v_or_b32_e32 v55, 35, v50
	v_or_b32_e32 v56, 40, v50
	v_or_b32_e32 v57, 41, v50
	v_or_b32_e32 v58, 42, v50
	v_or_b32_e32 v59, 43, v50
	v_or_b32_e32 v60, 48, v50
	v_or_b32_e32 v61, 49, v50
	v_or_b32_e32 v64, 50, v50
	v_or_b32_e32 v65, 51, v50
	v_or_b32_e32 v67, 56, v50
	v_or_b32_e32 v68, 57, v50
	v_or_b32_e32 v69, 58, v50
	v_or_b32_e32 v50, 59, v50
	v_cndmask_b32_e64 v49, 0, v49, s[30:31]
	v_cndmask_b32_e64 v48, 0, v48, s[28:29]
	v_cmp_lt_u32_e64 s[28:29], v69, v52
	v_cmp_lt_u32_e64 s[30:31], v50, v52
	v_cndmask_b32_e64 v47, 0, v47, s[26:27]
	v_cmp_lt_u32_e64 s[26:27], v68, v52
	s_or_b64 s[28:29], s[30:31], s[28:29]
	v_cndmask_b32_e64 v46, 0, v46, s[24:25]
	v_cmp_lt_u32_e64 s[24:25], v67, v52
	s_or_b64 s[26:27], s[28:29], s[26:27]
	v_cndmask_b32_e64 v45, 0, v45, s[22:23]
	v_cmp_lt_u32_e64 s[22:23], v65, v52
	s_or_b64 s[24:25], s[26:27], s[24:25]
	v_cndmask_b32_e64 v44, 0, v44, s[20:21]
	v_cmp_lt_u32_e64 s[20:21], v64, v52
	s_or_b64 s[22:23], s[24:25], s[22:23]
	v_cndmask_b32_e64 v43, 0, v43, s[18:19]
	v_cmp_lt_u32_e64 s[18:19], v61, v52
	s_or_b64 s[20:21], s[22:23], s[20:21]
	v_cndmask_b32_e64 v42, 0, v42, s[16:17]
	v_cmp_lt_u32_e64 s[16:17], v60, v52
	s_or_b64 s[18:19], s[20:21], s[18:19]
	v_cndmask_b32_e64 v41, 0, v41, s[10:11]
	v_cmp_lt_u32_e64 s[10:11], v59, v52
	s_or_b64 s[16:17], s[18:19], s[16:17]
	v_cndmask_b32_e64 v40, 0, v40, s[8:9]
	v_cmp_lt_u32_e64 s[8:9], v58, v52
	s_or_b64 s[10:11], s[16:17], s[10:11]
	v_cndmask_b32_e64 v39, 0, v39, s[6:7]
	v_cmp_lt_u32_e64 s[6:7], v57, v52
	s_or_b64 s[8:9], s[10:11], s[8:9]
	v_cndmask_b32_e64 v38, 0, v38, s[4:5]
	v_cndmask_b32_e32 v35, 0, v35, vcc
	s_or_b64 vcc, vcc, s[0:1]
	v_cmp_lt_u32_e64 s[4:5], v56, v52
	s_or_b64 s[6:7], s[8:9], s[6:7]
	v_cndmask_b32_e64 v37, 0, v37, s[2:3]
	v_cndmask_b32_e64 v18, 0, v18, s[0:1]
	v_cndmask_b32_e32 v34, 0, v34, vcc
	v_cmp_lt_u32_e32 vcc, v53, v52
	v_cmp_lt_u32_e64 s[0:1], v54, v52
	v_cmp_lt_u32_e64 s[2:3], v55, v52
	s_or_b64 s[4:5], s[6:7], s[4:5]
	v_and_b32_e32 v50, 19, v66
	v_lshlrev_b32_e32 v52, 1, v66
	s_or_b64 s[2:3], s[4:5], s[2:3]
	v_and_or_b32 v50, v52, 8, v50
	s_or_b64 s[0:1], s[2:3], s[0:1]
	v_and_b32_e32 v52, 8, v66
	v_lshlrev_b32_e32 v50, 1, v50
	v_cndmask_b32_e64 v20, 0, v20, s[0:1]
	s_or_b64 vcc, s[0:1], vcc
	v_add3_u32 v50, s48, v52, v50
	s_movk_i32 s0, 0x240
	v_cvt_pk_bf16_f32 v34, v34, v35
	v_mad_u32_u24 v193, v62, s0, v50
	ds_write_b16 v193, v34
	ds_write_b16_d16_hi v193, v34 offset:144
	v_cvt_pk_bf16_f32 v34, v36, v37
	v_mad_u32_u24 v195, v51, s83, v50
	ds_write_b16 v195, v34
	ds_write_b16_d16_hi v195, v34 offset:144
	v_cvt_pk_bf16_f32 v34, v38, v39
	ds_write_b16 v195, v34 offset:864
	ds_write_b16_d16_hi v195, v34 offset:1008
	v_cvt_pk_bf16_f32 v34, v40, v41
	ds_write_b16 v195, v34 offset:1152
	ds_write_b16_d16_hi v195, v34 offset:1296
	v_cvt_pk_bf16_f32 v34, v42, v43
	ds_write_b16 v195, v34 offset:2016
	ds_write_b16_d16_hi v195, v34 offset:2160
; #define R2_ZERO(M) do { _Pragma("unroll") for (int _a = 0; _a < 2; ++_a) _Pragma("unroll") for (int _b = 0; _b < 2; ++_b) _Pragma("unroll") for (int _r = 0; _r < 16; ++_r) M[_a][_b][_r] = 0.f; } while (0)
; #define R2_PACK(Bpk, M) do { _Pragma("unroll") for (int _ks = 0; _ks < 4; ++_ks) _Pragma("unroll") for (int _cb = 0; _cb < 2; ++_cb) Bpk[_ks][_cb] = pack_acc(M[_ks >> 1][_cb], _ks & 1); } while (0)
; __device__ __forceinline__ void ph_rwkv_chunk(const Params& p, int l, LAS unsigned char* lds, const int wvid) {
;     ...
;             R2_TO_LDS(X, A);
;             M64 Z; R2_ZERO(Z); R2_MM_LP(Z, X, Tpk); R2_PACK(Zpk, Z);
;         }
;         {
;             R2_RAW(X, VVg); R2_TRANS_L(Y, X);
	v_cvt_pk_bf16_f32 v34, v44, v45
	ds_write_b16 v195, v34 offset:2304
	ds_write_b16_d16_hi v195, v34 offset:2448
	v_cvt_pk_bf16_f32 v34, v46, v47
	ds_write_b16 v195, v34 offset:3168
	ds_write_b16_d16_hi v195, v34 offset:3312
	v_cvt_pk_bf16_f32 v34, v48, v49
	ds_write_b16 v195, v34 offset:3456
	ds_write_b16_d16_hi v195, v34 offset:3600
	ds_write_b16 v193, v2 offset:64
	ds_write_b16_d16_hi v193, v2 offset:208
	v_cvt_pk_bf16_f32 v2, v4, v5
	ds_write_b16 v195, v2 offset:64
	ds_write_b16_d16_hi v195, v2 offset:208
	v_cvt_pk_bf16_f32 v2, v6, v7
	ds_write_b16 v195, v2 offset:928
	ds_write_b16_d16_hi v195, v2 offset:1072
	v_cvt_pk_bf16_f32 v2, v8, v9
	ds_write_b16 v195, v2 offset:1216
	ds_write_b16_d16_hi v195, v2 offset:1360
	v_cvt_pk_bf16_f32 v2, v10, v11
	ds_write_b16 v195, v2 offset:2080
	ds_write_b16_d16_hi v195, v2 offset:2224
	v_cvt_pk_bf16_f32 v2, v12, v13
	ds_write_b16 v195, v2 offset:2368
	ds_write_b16_d16_hi v195, v2 offset:2512
	v_cvt_pk_bf16_f32 v2, v14, v15
	v_cndmask_b32_e32 v19, 0, v19, vcc
	ds_write_b16 v195, v2 offset:3232
	ds_write_b16_d16_hi v195, v2 offset:3376
	v_cvt_pk_bf16_f32 v2, v16, v17
	v_cndmask_b32_e64 v21, 0, v21, s[2:3]
	ds_write_b16 v195, v2 offset:3520
	ds_write_b16_d16_hi v195, v2 offset:3664
	ds_write_b16 v193, v1 offset:4608
	ds_write_b16 v193, v1 offset:4752
	v_mad_u32_u24 v194, v54, s83, v50
	v_cvt_pk_bf16_f32 v2, v18, v19
	v_cndmask_b32_e64 v23, 0, v23, s[6:7]
	v_cndmask_b32_e64 v22, 0, v22, s[4:5]
	ds_write_b16 v194, v1
	ds_write_b16 v194, v1 offset:144
	ds_write_b16 v194, v1 offset:864
	ds_write_b16 v194, v1 offset:1008
	ds_write_b16 v194, v1 offset:1152
	ds_write_b16 v194, v1 offset:1296
	ds_write_b16 v194, v1 offset:2016
	ds_write_b16 v194, v1 offset:2160
	ds_write_b16 v194, v1 offset:2304
	ds_write_b16 v194, v1 offset:2448
	ds_write_b16 v194, v1 offset:3168
	ds_write_b16 v194, v1 offset:3312
	ds_write_b16 v194, v1 offset:3456
	ds_write_b16 v194, v1 offset:3600
	ds_write_b16 v193, v2 offset:4672
	ds_write_b16_d16_hi v193, v2 offset:4816
	v_cvt_pk_bf16_f32 v2, v20, v21
	v_cndmask_b32_e64 v25, 0, v25, s[10:11]
	v_cndmask_b32_e64 v24, 0, v24, s[8:9]
	ds_write_b16 v194, v2 offset:64
	ds_write_b16_d16_hi v194, v2 offset:208
	v_cvt_pk_bf16_f32 v2, v22, v23
	v_cndmask_b32_e64 v27, 0, v27, s[18:19]
	v_cndmask_b32_e64 v26, 0, v26, s[16:17]
	ds_write_b16 v194, v2 offset:928
	ds_write_b16_d16_hi v194, v2 offset:1072
	v_cvt_pk_bf16_f32 v2, v24, v25
	v_cndmask_b32_e64 v29, 0, v29, s[22:23]
	v_cndmask_b32_e64 v28, 0, v28, s[20:21]
	ds_write_b16 v194, v2 offset:1216
	ds_write_b16_d16_hi v194, v2 offset:1360
	v_cvt_pk_bf16_f32 v2, v26, v27
	v_cndmask_b32_e64 v31, 0, v31, s[26:27]
	v_cndmask_b32_e64 v30, 0, v30, s[24:25]
	ds_write_b16 v194, v2 offset:2080
	ds_write_b16_d16_hi v194, v2 offset:2224
	v_cvt_pk_bf16_f32 v2, v28, v29
	v_cndmask_b32_e64 v33, 0, v33, s[30:31]
	v_cndmask_b32_e64 v32, 0, v32, s[28:29]
	ds_write_b16 v194, v2 offset:2368
	ds_write_b16_d16_hi v194, v2 offset:2512
	v_cvt_pk_bf16_f32 v2, v30, v31
	ds_write_b16 v194, v2 offset:3232
	ds_write_b16_d16_hi v194, v2 offset:3376
	v_cvt_pk_bf16_f32 v2, v32, v33
	ds_write_b16 v194, v2 offset:3520
	ds_write_b16_d16_hi v194, v2 offset:3664
	v_mul_u32_u24_e32 v0, 0x90, v0
	v_add3_u32 v196, s48, v63, v0
	ds_read_b128 v[2:5], v196
	ds_read_b128 v[68:71], v196 offset:32
	s_waitcnt lgkmcnt(1)
	v_mfma_f32_32x32x16_bf16 v[50:65], v[2:5], v[162:165], 0
	v_and_b32_e32 v67, 63, v66
	v_lshlrev_b32_e32 v0, 4, v67
	v_lshl_add_u64 v[88:89], s[42:43], 0, v[0:1]
	v_add_co_u32_e32 v100, vcc, s44, v88
	s_nop 1
	v_addc_co_u32_e32 v101, vcc, 0, v89, vcc
	v_mfma_f32_32x32x16_bf16 v[34:49], v[2:5], v[166:169], 0
	ds_read_b128 v[2:5], v196 offset:4608
	s_waitcnt lgkmcnt(1)
	v_mfma_f32_32x32x16_bf16 v[50:65], v[68:71], v[154:157], v[50:65]
	v_mfma_f32_32x32x16_bf16 v[34:49], v[68:71], v[158:161], v[34:49]
	ds_read_b128 v[68:71], v196 offset:4640
	s_waitcnt lgkmcnt(1)
	v_mfma_f32_32x32x16_bf16 v[18:33], v[2:5], v[162:165], 0
	v_mfma_f32_32x32x16_bf16 v[2:17], v[2:5], v[166:169], 0
	s_waitcnt lgkmcnt(0)
	v_mfma_f32_32x32x16_bf16 v[18:33], v[68:71], v[154:157], v[18:33]
	v_mfma_f32_32x32x16_bf16 v[2:17], v[68:71], v[158:161], v[2:17]
	ds_read_b128 v[68:71], v196 offset:64
	s_waitcnt lgkmcnt(0)
	v_mfma_f32_32x32x16_bf16 v[50:65], v[68:71], v[182:185], v[50:65]
	v_mfma_f32_32x32x16_bf16 v[34:49], v[68:71], v[186:189], v[34:49]
	ds_read_b128 v[68:71], v196 offset:4672
	s_waitcnt lgkmcnt(0)
	v_mfma_f32_32x32x16_bf16 v[18:33], v[68:71], v[182:185], v[18:33]
	v_mfma_f32_32x32x16_bf16 v[2:17], v[68:71], v[186:189], v[2:17]
	ds_read_b128 v[68:71], v196 offset:96
	s_waitcnt lgkmcnt(0)
	v_mfma_f32_32x32x16_bf16 v[50:65], v[68:71], v[178:181], v[50:65]
	v_mfma_f32_32x32x16_bf16 v[34:49], v[68:71], v[150:153], v[34:49]
	ds_read_b128 v[68:71], v196 offset:4704
	global_load_dwordx4 v[72:75], v0, s[42:43]
	global_load_dwordx4 v[76:79], v0, s[42:43] offset:1024
	global_load_dwordx4 v[80:83], v0, s[42:43] offset:2048
	global_load_dwordx4 v[84:87], v0, s[42:43] offset:3072
	global_load_dwordx4 v[88:91], v[100:101], off
	global_load_dwordx4 v[92:95], v[100:101], off offset:1024
	global_load_dwordx4 v[96:99], v[100:101], off offset:2048
	s_nop 0
	global_load_dwordx4 v[100:103], v[100:101], off offset:3072
	v_lshlrev_b32_e32 v0, 4, v66
	v_bfe_u32 v66, v66, 1, 5
	v_and_b32_e32 v0, 16, v0
	v_mul_u32_u24_e32 v66, 0x90, v66
	v_add3_u32 v0, s48, v66, v0
	s_waitcnt vmcnt(7)
	ds_write_b128 v0, v[72:75]
	s_waitcnt vmcnt(6)
	ds_write_b128 v0, v[76:79] offset:4608
	s_waitcnt vmcnt(5)
	ds_write_b128 v0, v[80:83] offset:32
	s_waitcnt vmcnt(4)
	ds_write_b128 v0, v[84:87] offset:4640
	s_waitcnt vmcnt(3)
; #define R2_ZERO(M) do { _Pragma("unroll") for (int _a = 0; _a < 2; ++_a) _Pragma("unroll") for (int _b = 0; _b < 2; ++_b) _Pragma("unroll") for (int _r = 0; _r < 16; ++_r) M[_a][_b][_r] = 0.f; } while (0)
; #define R2_PACK(Bpk, M) do { _Pragma("unroll") for (int _ks = 0; _ks < 4; ++_ks) _Pragma("unroll") for (int _cb = 0; _cb < 2; ++_cb) Bpk[_ks][_cb] = pack_acc(M[_ks >> 1][_cb], _ks & 1); } while (0)
; __device__ __forceinline__ void ph_rwkv_chunk(const Params& p, int l, LAS unsigned char* lds, const int wvid) {
;     ...
;             M64 Z; R2_ZERO(Z); R2_MM_LP(Z, X, Tpk); R2_PACK(Zpk, Z);
;         }
;         {
;             R2_RAW(X, VVg); R2_TRANS_L(Y, X);
;             M64 W; R2_ZERO(W); R2_MM_LP(W, Y, Zpk);
;             asm volatile("" ::: "memory");
;             R2_TO_LDS(X, W);
	ds_write_b128 v0, v[88:91] offset:64
	s_waitcnt vmcnt(2)
	ds_write_b128 v0, v[92:95] offset:4672
	s_waitcnt vmcnt(1)
	ds_write_b128 v0, v[96:99] offset:96
	s_waitcnt vmcnt(0)
	ds_write_b128 v0, v[100:103] offset:4704
	v_lshl_add_u32 v0, v67, 1, s48
	s_waitcnt lgkmcnt(8)
	v_mfma_f32_32x32x16_bf16 v[18:33], v[68:71], v[178:181], v[18:33]
	v_cvt_pk_bf16_f32 v34, v34, v35
	v_cvt_pk_bf16_f32 v35, v36, v37
	v_cvt_pk_bf16_f32 v36, v38, v39
	v_cvt_pk_bf16_f32 v37, v40, v41
	v_cvt_pk_bf16_f32 v50, v50, v51
	v_cvt_pk_bf16_f32 v51, v52, v53
	v_cvt_pk_bf16_f32 v52, v54, v55
	v_mfma_f32_32x32x16_bf16 v[2:17], v[68:71], v[150:153], v[2:17]
	v_mad_u32_u24 v70, v67, s83, v191
	ds_read_u16 v66, v0
	ds_read_u16 v67, v0 offset:144
	ds_read_u16 v68, v0 offset:288
	ds_read_u16 v69, v0 offset:432
	ds_read_u16 v71, v0 offset:576
	ds_read_u16 v72, v0 offset:720
	ds_read_u16 v73, v0 offset:864
	ds_read_u16 v74, v0 offset:1008
	s_waitcnt lgkmcnt(6)
	v_lshl_or_b32 v66, v67, 16, v66
	s_waitcnt lgkmcnt(4)
	v_lshl_or_b32 v67, v69, 16, v68
	ds_read_u16 v68, v0 offset:1152
	ds_read_u16 v69, v0 offset:1296
	ds_read_u16 v75, v0 offset:1440
	ds_read_u16 v76, v0 offset:1584
	ds_read_u16 v77, v0 offset:1728
	ds_read_u16 v78, v0 offset:1872
	ds_read_u16 v79, v0 offset:2016
	ds_read_u16 v80, v0 offset:2160
	s_waitcnt lgkmcnt(6)
	v_lshl_or_b32 v68, v69, 16, v68
	s_waitcnt lgkmcnt(4)
	v_lshl_or_b32 v69, v76, 16, v75
	ds_write_b128 v70, v[66:69] offset:9216
	v_lshl_or_b32 v66, v72, 16, v71
	v_lshl_or_b32 v67, v74, 16, v73
	s_waitcnt lgkmcnt(3)
	v_lshl_or_b32 v68, v78, 16, v77
	s_waitcnt lgkmcnt(1)
	v_lshl_or_b32 v69, v80, 16, v79
	ds_write_b128 v70, v[66:69] offset:9232
	ds_read_u16 v66, v0 offset:2304
	ds_read_u16 v67, v0 offset:2448
	ds_read_u16 v68, v0 offset:2592
	ds_read_u16 v69, v0 offset:2736
	ds_read_u16 v71, v0 offset:2880
	ds_read_u16 v72, v0 offset:3024
	ds_read_u16 v73, v0 offset:3168
	ds_read_u16 v74, v0 offset:3312
	s_waitcnt lgkmcnt(6)
	v_lshl_or_b32 v66, v67, 16, v66
	s_waitcnt lgkmcnt(4)
	v_lshl_or_b32 v67, v69, 16, v68
	ds_read_u16 v68, v0 offset:3456
	ds_read_u16 v69, v0 offset:3600
	ds_read_u16 v75, v0 offset:3744
	ds_read_u16 v76, v0 offset:3888
	ds_read_u16 v77, v0 offset:4032
	ds_read_u16 v78, v0 offset:4176
	ds_read_u16 v79, v0 offset:4320
	ds_read_u16 v80, v0 offset:4464
	s_waitcnt lgkmcnt(6)
	v_lshl_or_b32 v68, v69, 16, v68
	s_waitcnt lgkmcnt(4)
	v_lshl_or_b32 v69, v76, 16, v75
	ds_write_b128 v70, v[66:69] offset:9248
	v_lshl_or_b32 v66, v72, 16, v71
	v_lshl_or_b32 v67, v74, 16, v73
	s_waitcnt lgkmcnt(3)
	v_lshl_or_b32 v68, v78, 16, v77
	s_waitcnt lgkmcnt(1)
	v_lshl_or_b32 v69, v80, 16, v79
	ds_write_b128 v70, v[66:69] offset:9264
	ds_read_u16 v66, v0 offset:4608
	ds_read_u16 v67, v0 offset:4752
	ds_read_u16 v68, v0 offset:4896
	ds_read_u16 v69, v0 offset:5040
	ds_read_u16 v71, v0 offset:5184
	ds_read_u16 v72, v0 offset:5328
	ds_read_u16 v73, v0 offset:5472
	ds_read_u16 v74, v0 offset:5616
	s_waitcnt lgkmcnt(6)
	v_lshl_or_b32 v66, v67, 16, v66
	s_waitcnt lgkmcnt(4)
	v_lshl_or_b32 v67, v69, 16, v68
	ds_read_u16 v68, v0 offset:5760
	ds_read_u16 v69, v0 offset:5904
	ds_read_u16 v75, v0 offset:6048
	ds_read_u16 v76, v0 offset:6192
	ds_read_u16 v77, v0 offset:6336
	ds_read_u16 v78, v0 offset:6480
	ds_read_u16 v79, v0 offset:6624
	ds_read_u16 v80, v0 offset:6768
	s_waitcnt lgkmcnt(6)
	v_lshl_or_b32 v68, v69, 16, v68
	s_waitcnt lgkmcnt(4)
	v_lshl_or_b32 v69, v76, 16, v75
	ds_write_b128 v70, v[66:69] offset:9280
	v_lshl_or_b32 v66, v72, 16, v71
	v_lshl_or_b32 v67, v74, 16, v73
	s_waitcnt lgkmcnt(3)
	v_lshl_or_b32 v68, v78, 16, v77
	s_waitcnt lgkmcnt(1)
	v_lshl_or_b32 v69, v80, 16, v79
	ds_write_b128 v70, v[66:69] offset:9296
	ds_read_u16 v66, v0 offset:6912
	ds_read_u16 v67, v0 offset:7056
	ds_read_u16 v68, v0 offset:7200
	ds_read_u16 v69, v0 offset:7344
	ds_read_u16 v71, v0 offset:7488
	ds_read_u16 v72, v0 offset:7632
	ds_read_u16 v73, v0 offset:7776
	ds_read_u16 v74, v0 offset:7920
	s_waitcnt lgkmcnt(6)
	v_lshl_or_b32 v66, v67, 16, v66
	s_waitcnt lgkmcnt(4)
	v_lshl_or_b32 v67, v69, 16, v68
	ds_read_u16 v68, v0 offset:8064
	ds_read_u16 v69, v0 offset:8208
	ds_read_u16 v75, v0 offset:8352
	ds_read_u16 v76, v0 offset:8496
	ds_read_u16 v77, v0 offset:8640
	ds_read_u16 v78, v0 offset:8784
	ds_read_u16 v79, v0 offset:8928
	ds_read_u16 v0, v0 offset:9072
	s_waitcnt lgkmcnt(6)
	v_lshl_or_b32 v68, v69, 16, v68
	s_waitcnt lgkmcnt(4)
	v_lshl_or_b32 v69, v76, 16, v75
	ds_write_b128 v70, v[66:69] offset:9312
	v_lshl_or_b32 v66, v72, 16, v71
	v_lshl_or_b32 v67, v74, 16, v73
	s_waitcnt lgkmcnt(3)
	v_lshl_or_b32 v68, v78, 16, v77
	s_waitcnt lgkmcnt(1)
	v_lshl_or_b32 v69, v0, 16, v79
	ds_write_b128 v70, v[66:69] offset:9328
	ds_read_b128 v[66:69], v196 offset:9216
	ds_read_b128 v[38:41], v196 offset:13824
	v_cvt_pk_bf16_f32 v53, v56, v57
	s_waitcnt lgkmcnt(1)
	v_mfma_f32_32x32x16_bf16 v[98:113], v[66:69], v[34:37], 0
	v_cvt_pk_bf16_f32 v42, v42, v43
	v_cvt_pk_bf16_f32 v43, v44, v45
	v_cvt_pk_bf16_f32 v44, v46, v47
	v_cvt_pk_bf16_f32 v45, v48, v49
	v_cvt_pk_bf16_f32 v2, v2, v3
	v_cvt_pk_bf16_f32 v3, v4, v5
	v_cvt_pk_bf16_f32 v4, v6, v7
	v_mfma_f32_32x32x16_bf16 v[114:129], v[66:69], v[50:53], 0
	v_cvt_pk_bf16_f32 v5, v8, v9
	ds_read_b128 v[6:9], v196 offset:13888
	v_cvt_pk_bf16_f32 v18, v18, v19
	v_cvt_pk_bf16_f32 v19, v20, v21
	v_cvt_pk_bf16_f32 v20, v22, v23
	v_cvt_pk_bf16_f32 v21, v24, v25
	v_cvt_pk_bf16_f32 v10, v10, v11
	s_waitcnt lgkmcnt(1)
	v_mfma_f32_32x32x16_bf16 v[66:81], v[38:41], v[34:37], 0
	ds_read_b128 v[34:37], v196 offset:9248
	v_cvt_pk_bf16_f32 v11, v12, v13
	v_cvt_pk_bf16_f32 v12, v14, v15
	v_cvt_pk_bf16_f32 v13, v16, v17
	v_mfma_f32_32x32x16_bf16 v[82:97], v[38:41], v[50:53], 0
	v_cvt_pk_bf16_f32 v38, v58, v59
	v_cvt_pk_bf16_f32 v39, v60, v61
	v_cvt_pk_bf16_f32 v40, v62, v63
	v_cvt_pk_bf16_f32 v41, v64, v65
	s_waitcnt lgkmcnt(0)
; #define R2_ZERO(M) do { _Pragma("unroll") for (int _a = 0; _a < 2; ++_a) _Pragma("unroll") for (int _b = 0; _b < 2; ++_b) _Pragma("unroll") for (int _r = 0; _r < 16; ++_r) M[_a][_b][_r] = 0.f; } while (0)
; #define R2_PACK(Bpk, M) do { _Pragma("unroll") for (int _ks = 0; _ks < 4; ++_ks) _Pragma("unroll") for (int _cb = 0; _cb < 2; ++_cb) Bpk[_ks][_cb] = pack_acc(M[_ks >> 1][_cb], _ks & 1); } while (0)
; #define R2_MASK(M, STRICT) do { _Pragma("unroll") for (int _rb = 0; _rb < 2; ++_rb) _Pragma("unroll") for (int _cb = 0; _cb < 2; ++_cb) _Pragma("unroll") for (int _r = 0; _r < 16; ++_r) { \
;         const int _row = 32 * _rb + (_r & 3) + 8 * (_r >> 2) + 4 * hi, _col = 32 * _cb + l31; if (STRICT ? !(_row < _col) : !(_row <= _col)) M[_rb][_cb][_r] = 0.f; } } while (0)
; #define R2_RELANE() do { lane = lt_tid(wvid) & 63; l31 = lane & 31; hi = lane >> 5; } while (0)
; __device__ __forceinline__ void ph_rwkv_chunk(const Params& p, int l, LAS unsigned char* lds, const int wvid) {
;     ...
;             M64 W; R2_ZERO(W); R2_MM_LP(W, Y, Zpk);
;             asm volatile("" ::: "memory");
;             R2_TO_LDS(X, W);
;         }
;         R2_RELANE();
;         {
;             bf16x8 AKR[4][2];
;             { M64 B; R2_ZERO(B); R2_MM_GG(B, KTg, RTg); R2_MASK(B, false); R2_PACK(AKR, B); }
	s_nop 0
	v_mfma_f32_32x32x16_bf16 v[114:129], v[34:37], v[38:41], v[114:129]
	v_mfma_f32_32x32x16_bf16 v[98:113], v[34:37], v[42:45], v[98:113]
	ds_read_b128 v[34:37], v196 offset:13856
	s_waitcnt lgkmcnt(0)
	v_mfma_f32_32x32x16_bf16 v[82:97], v[34:37], v[38:41], v[82:97]
	v_mfma_f32_32x32x16_bf16 v[66:81], v[34:37], v[42:45], v[66:81]
	ds_read_b128 v[34:37], v196 offset:9280
	s_waitcnt lgkmcnt(0)
	v_mfma_f32_32x32x16_bf16 v[98:113], v[34:37], v[2:5], v[98:113]
	v_mfma_f32_32x32x16_bf16 v[66:81], v[6:9], v[2:5], v[66:81]
	ds_read_b128 v[2:5], v196 offset:9312
	v_mfma_f32_32x32x16_bf16 v[114:129], v[34:37], v[18:21], v[114:129]
	v_mfma_f32_32x32x16_bf16 v[82:97], v[6:9], v[18:21], v[82:97]
	v_cvt_pk_bf16_f32 v6, v26, v27
	v_cvt_pk_bf16_f32 v7, v28, v29
	v_cvt_pk_bf16_f32 v8, v30, v31
	v_cvt_pk_bf16_f32 v9, v32, v33
	s_waitcnt lgkmcnt(0)
	s_nop 0
	v_mfma_f32_32x32x16_bf16 v[114:129], v[2:5], v[6:9], v[114:129]
	v_mfma_f32_32x32x16_bf16 v[98:113], v[2:5], v[10:13], v[98:113]
	ds_read_b128 v[2:5], v196 offset:13920
	s_nop 9
	v_cvt_pk_bf16_f32 v0, v114, v115
	ds_write_b16 v193, v0
	ds_write_b16_d16_hi v193, v0 offset:144
	v_cvt_pk_bf16_f32 v0, v116, v117
	ds_write_b16 v195, v0
	ds_write_b16_d16_hi v195, v0 offset:144
	v_cvt_pk_bf16_f32 v0, v118, v119
	ds_write_b16 v195, v0 offset:864
	ds_write_b16_d16_hi v195, v0 offset:1008
	v_cvt_pk_bf16_f32 v0, v120, v121
	ds_write_b16 v195, v0 offset:1152
	ds_write_b16_d16_hi v195, v0 offset:1296
	v_cvt_pk_bf16_f32 v0, v122, v123
	ds_write_b16 v195, v0 offset:2016
	ds_write_b16_d16_hi v195, v0 offset:2160
	v_cvt_pk_bf16_f32 v0, v124, v125
	ds_write_b16 v195, v0 offset:2304
	ds_write_b16_d16_hi v195, v0 offset:2448
	v_cvt_pk_bf16_f32 v0, v126, v127
	ds_write_b16 v195, v0 offset:3168
	ds_write_b16_d16_hi v195, v0 offset:3312
	v_cvt_pk_bf16_f32 v0, v128, v129
	s_waitcnt lgkmcnt(14)
	v_mfma_f32_32x32x16_bf16 v[82:97], v[2:5], v[6:9], v[82:97]
	ds_write_b16 v195, v0 offset:3456
	ds_write_b16_d16_hi v195, v0 offset:3600
	v_cvt_pk_bf16_f32 v0, v98, v99
	ds_write_b16 v193, v0 offset:64
	ds_write_b16_d16_hi v193, v0 offset:208
	v_cvt_pk_bf16_f32 v0, v100, v101
	ds_write_b16 v195, v0 offset:64
	ds_write_b16_d16_hi v195, v0 offset:208
	v_cvt_pk_bf16_f32 v0, v102, v103
	ds_write_b16 v195, v0 offset:928
	ds_write_b16_d16_hi v195, v0 offset:1072
	v_cvt_pk_bf16_f32 v0, v104, v105
	ds_write_b16 v195, v0 offset:1216
	ds_write_b16_d16_hi v195, v0 offset:1360
	v_cvt_pk_bf16_f32 v0, v106, v107
	ds_write_b16 v195, v0 offset:2080
	ds_write_b16_d16_hi v195, v0 offset:2224
	v_cvt_pk_bf16_f32 v0, v108, v109
	ds_write_b16 v195, v0 offset:2368
	ds_write_b16_d16_hi v195, v0 offset:2512
	v_cvt_pk_bf16_f32 v0, v110, v111
	ds_write_b16 v195, v0 offset:3232
	ds_write_b16_d16_hi v195, v0 offset:3376
	v_cvt_pk_bf16_f32 v0, v112, v113
	v_mfma_f32_32x32x16_bf16 v[66:81], v[2:5], v[10:13], v[66:81]
	ds_write_b16 v195, v0 offset:3520
	ds_write_b16_d16_hi v195, v0 offset:3664
	v_cvt_pk_bf16_f32 v0, v82, v83
	ds_write_b16 v193, v0 offset:4608
	ds_write_b16_d16_hi v193, v0 offset:4752
	v_cvt_pk_bf16_f32 v0, v84, v85
	ds_write_b16 v194, v0
	ds_write_b16_d16_hi v194, v0 offset:144
	v_cvt_pk_bf16_f32 v0, v86, v87
	ds_write_b16 v194, v0 offset:864
	ds_write_b16_d16_hi v194, v0 offset:1008
	v_cvt_pk_bf16_f32 v0, v88, v89
	ds_write_b16 v194, v0 offset:1152
	ds_write_b16_d16_hi v194, v0 offset:1296
	v_cvt_pk_bf16_f32 v0, v90, v91
	ds_write_b16 v194, v0 offset:2016
	ds_write_b16_d16_hi v194, v0 offset:2160
	v_cvt_pk_bf16_f32 v0, v92, v93
	ds_write_b16 v194, v0 offset:2304
	ds_write_b16_d16_hi v194, v0 offset:2448
	v_cvt_pk_bf16_f32 v0, v94, v95
	ds_write_b16 v194, v0 offset:3168
	ds_write_b16_d16_hi v194, v0 offset:3312
	v_cvt_pk_bf16_f32 v0, v96, v97
	ds_write_b16 v194, v0 offset:3456
	ds_write_b16_d16_hi v194, v0 offset:3600
	v_cvt_pk_bf16_f32 v0, v66, v67
	ds_write_b16 v193, v0 offset:4672
	ds_write_b16_d16_hi v193, v0 offset:4816
	v_cvt_pk_bf16_f32 v0, v68, v69
	ds_write_b16 v194, v0 offset:64
	ds_write_b16_d16_hi v194, v0 offset:208
	v_cvt_pk_bf16_f32 v0, v70, v71
	ds_write_b16 v194, v0 offset:928
	ds_write_b16_d16_hi v194, v0 offset:1072
	v_cvt_pk_bf16_f32 v0, v72, v73
	ds_write_b16 v194, v0 offset:1216
	ds_write_b16_d16_hi v194, v0 offset:1360
	v_cvt_pk_bf16_f32 v0, v74, v75
	ds_write_b16 v194, v0 offset:2080
	ds_write_b16_d16_hi v194, v0 offset:2224
	v_cvt_pk_bf16_f32 v0, v76, v77
	ds_write_b16 v194, v0 offset:2368
	ds_write_b16_d16_hi v194, v0 offset:2512
	v_cvt_pk_bf16_f32 v0, v78, v79
	ds_write_b16 v194, v0 offset:3232
	ds_write_b16_d16_hi v194, v0 offset:3376
	v_cvt_pk_bf16_f32 v0, v80, v81
	ds_write_b16 v194, v0 offset:3520
	ds_write_b16_d16_hi v194, v0 offset:3664
	v_mbcnt_lo_u32_b32 v2, -1, 0
	v_mbcnt_hi_u32_b32 v2, -1, v2
	s_nop 0
	v_or_b32_e32 v0, s75, v2
	v_and_b32_e32 v115, 31, v2
	v_bfe_u32 v124, v0, 5, 1
	v_lshlrev_b32_e32 v114, 5, v115
	v_lshlrev_b32_e32 v14, 4, v124
	v_or_b32_e32 v15, v14, v114
	v_or_b32_e32 v184, 0x1000, v15
	v_or_b32_e32 v185, 0x1400, v15
	v_or_b32_e32 v186, 0x1800, v15
	v_or_b32_e32 v187, 0x1c00, v15
	global_load_dwordx4 v[36:39], v15, s[36:37]
	global_load_dwordx4 v[40:43], v15, s[54:55]
	global_load_dwordx4 v[44:47], v15, s[54:55] offset:1024
	global_load_dwordx4 v[48:51], v15, s[36:37] offset:1024
	global_load_dwordx4 v[52:55], v15, s[36:37] offset:2048
	global_load_dwordx4 v[56:59], v15, s[54:55] offset:2048
	global_load_dwordx4 v[60:63], v15, s[36:37] offset:3072
	global_load_dwordx4 v[64:67], v15, s[54:55] offset:3072
	global_load_dwordx4 v[68:71], v184, s[36:37]
	global_load_dwordx4 v[72:75], v184, s[54:55]
	global_load_dwordx4 v[76:79], v185, s[54:55]
	global_load_dwordx4 v[116:119], v185, s[36:37]
	global_load_dwordx4 v[120:123], v186, s[36:37]
	global_load_dwordx4 v[232:235], v186, s[54:55]
	global_load_dwordx4 v[236:239], v187, s[54:55]
	global_load_dwordx4 v[240:243], v187, s[36:37]
	s_waitcnt vmcnt(0)
; #define R2_ZERO(M) do { _Pragma("unroll") for (int _a = 0; _a < 2; ++_a) _Pragma("unroll") for (int _b = 0; _b < 2; ++_b) _Pragma("unroll") for (int _r = 0; _r < 16; ++_r) M[_a][_b][_r] = 0.f; } while (0)
; #define R2_PACK(Bpk, M) do { _Pragma("unroll") for (int _ks = 0; _ks < 4; ++_ks) _Pragma("unroll") for (int _cb = 0; _cb < 2; ++_cb) Bpk[_ks][_cb] = pack_acc(M[_ks >> 1][_cb], _ks & 1); } while (0)
; #define R2_MASK(M, STRICT) do { _Pragma("unroll") for (int _rb = 0; _rb < 2; ++_rb) _Pragma("unroll") for (int _cb = 0; _cb < 2; ++_cb) _Pragma("unroll") for (int _r = 0; _r < 16; ++_r) { \
;         const int _row = 32 * _rb + (_r & 3) + 8 * (_r >> 2) + 4 * hi, _col = 32 * _cb + l31; if (STRICT ? !(_row < _col) : !(_row <= _col)) M[_rb][_cb][_r] = 0.f; } } while (0)
; __device__ __forceinline__ void ph_rwkv_chunk(const Params& p, int l, LAS unsigned char* lds, const int wvid) {
;     ...
;             { M64 B; R2_ZERO(B); R2_MM_GG(B, KTg, RTg); R2_MASK(B, false); R2_PACK(AKR, B); }
;             M64 Yl; R2_ZERO(Yl); R2_MM_LP(Yl, X, ABR); R2_MM_LP(Yl, Y, AKR);
	v_mfma_f32_32x32x16_bf16 v[82:97], v[36:39], v[40:43], 0
	v_or_b32_e32 v16, 0x1000, v15
	v_lshlrev_b32_e32 v124, 2, v124
	v_cmp_gt_u32_e32 vcc, v124, v115
	v_cmp_lt_u32_e64 s[0:1], v124, v115
	v_lshrrev_b32_e32 v0, 1, v0
	v_and_or_b32 v0, v0, 16, v114
	s_waitcnt vmcnt(0)
	v_mfma_f32_32x32x16_bf16 v[98:113], v[36:39], v[44:47], 0
	s_waitcnt vmcnt(1)
	v_mfma_f32_32x32x16_bf16 v[18:33], v[48:51], v[44:47], 0
	s_waitcnt vmcnt(1)
	v_mfma_f32_32x32x16_bf16 v[82:97], v[52:55], v[56:59], v[82:97]
	s_waitcnt vmcnt(0)
	v_mfma_f32_32x32x16_bf16 v[98:113], v[52:55], v[64:67], v[98:113]
	v_mfma_f32_32x32x16_bf16 v[18:33], v[60:63], v[64:67], v[18:33]
	v_or_b32_e32 v6, 0x1400, v15
	v_or_b32_e32 v16, 0x1800, v15
	s_waitcnt vmcnt(0)
	v_mfma_f32_32x32x16_bf16 v[82:97], v[68:71], v[72:75], v[82:97]
	s_nop 0
	s_waitcnt vmcnt(1)
	v_mfma_f32_32x32x16_bf16 v[98:113], v[68:71], v[76:79], v[98:113]
	s_waitcnt vmcnt(1)
	v_mfma_f32_32x32x16_bf16 v[18:33], v[116:119], v[76:79], v[18:33]
	v_or_b32_e32 v6, 0x1c00, v15
	s_waitcnt vmcnt(0)
	v_mfma_f32_32x32x16_bf16 v[82:97], v[120:123], v[232:235], v[82:97]
	s_nop 10
	v_cndmask_b32_e64 v126, v82, 0, vcc
	s_waitcnt vmcnt(1)
	v_mfma_f32_32x32x16_bf16 v[98:113], v[120:123], v[236:239], v[98:113]
	v_cndmask_b32_e64 v126, v126, v82, s[0:1]
	v_or_b32_e32 v82, 2, v124
	v_cndmask_b32_e64 v127, 0, v83, s[0:1]
	v_cmp_le_u32_e64 s[0:1], v82, v115
	v_or_b32_e32 v82, 3, v124
	s_waitcnt vmcnt(0)
	v_mfma_f32_32x32x16_bf16 v[18:33], v[240:243], v[236:239], v[18:33]
	v_mul_u32_u24_e32 v2, 0x90, v115
	v_add3_u32 v125, s48, v14, v2
	ds_read_b128 v[2:5], v125
	ds_read_b128 v[116:119], v125 offset:32
	v_cndmask_b32_e64 v128, 0, v84, s[0:1]
	v_cmp_le_u32_e64 s[0:1], v82, v115
	v_or_b32_e32 v82, 8, v124
	s_waitcnt lgkmcnt(1)
	v_mfma_f32_32x32x16_bf16 v[66:81], v[2:5], v[134:137], 0
	v_cvt_pk_bf16_f32 v98, v98, v99
	v_cvt_pk_bf16_f32 v99, v100, v101
	v_cvt_pk_bf16_f32 v100, v102, v103
	v_cvt_pk_bf16_f32 v101, v104, v105
	v_cndmask_b32_e64 v18, v18, 0, vcc
	v_mfma_f32_32x32x16_bf16 v[50:65], v[2:5], v[138:141], 0
	ds_read_b128 v[2:5], v125 offset:4608
	s_waitcnt lgkmcnt(1)
	v_mfma_f32_32x32x16_bf16 v[66:81], v[116:119], v[142:145], v[66:81]
	v_mfma_f32_32x32x16_bf16 v[50:65], v[116:119], v[146:149], v[50:65]
	ds_read_b128 v[116:119], v125 offset:4640
	s_waitcnt lgkmcnt(1)
	v_mfma_f32_32x32x16_bf16 v[34:49], v[2:5], v[134:137], 0
	v_mfma_f32_32x32x16_bf16 v[2:17], v[2:5], v[138:141], 0
	s_waitcnt lgkmcnt(0)
	v_mfma_f32_32x32x16_bf16 v[34:49], v[116:119], v[142:145], v[34:49]
	v_mfma_f32_32x32x16_bf16 v[2:17], v[116:119], v[146:149], v[2:17]
	ds_read_b128 v[116:119], v125 offset:64
	s_waitcnt lgkmcnt(0)
	v_mfma_f32_32x32x16_bf16 v[66:81], v[116:119], v[130:133], v[66:81]
	v_mfma_f32_32x32x16_bf16 v[50:65], v[116:119], v[170:173], v[50:65]
	ds_read_b128 v[116:119], v125 offset:4672
	s_waitcnt lgkmcnt(0)
	v_mfma_f32_32x32x16_bf16 v[34:49], v[116:119], v[130:133], v[34:49]
	v_mfma_f32_32x32x16_bf16 v[2:17], v[116:119], v[170:173], v[2:17]
	ds_read_b128 v[116:119], v125 offset:96
	ds_read_b128 v[120:123], v125 offset:4704
	ds_read_b128 v[102:105], v125 offset:13824
	s_waitcnt lgkmcnt(2)
	v_mfma_f32_32x32x16_bf16 v[66:81], v[116:119], v[130:133], v[66:81]
	v_mfma_f32_32x32x16_bf16 v[50:65], v[116:119], v[174:177], v[50:65]
	v_cndmask_b32_e64 v116, 0, v85, s[0:1]
	v_cmp_le_u32_e64 s[0:1], v82, v115
	v_or_b32_e32 v82, 9, v124
	s_nop 0
	v_cndmask_b32_e64 v117, 0, v86, s[0:1]
	v_cmp_le_u32_e64 s[0:1], v82, v115
	v_or_b32_e32 v82, 10, v124
	s_waitcnt lgkmcnt(1)
	v_mfma_f32_32x32x16_bf16 v[34:49], v[120:123], v[130:133], v[34:49]
	v_cndmask_b32_e64 v118, 0, v87, s[0:1]
	v_cmp_le_u32_e64 s[0:1], v82, v115
	v_or_b32_e32 v82, 11, v124
	v_or_b32_e32 v86, 16, v124
	v_cndmask_b32_e64 v119, 0, v88, s[0:1]
	v_cmp_le_u32_e64 s[0:1], v82, v115
	ds_read_b128 v[82:85], v125 offset:9216
	v_mfma_f32_32x32x16_bf16 v[2:17], v[120:123], v[174:177], v[2:17]
	v_cndmask_b32_e64 v89, 0, v89, s[0:1]
	v_cmp_le_u32_e64 s[0:1], v86, v115
	v_or_b32_e32 v120, 17, v124
	v_cvt_pk_bf16_f32 v86, v126, v127
	v_cvt_pk_bf16_f32 v87, v128, v116
	v_cvt_pk_bf16_f32 v88, v117, v118
	v_cvt_pk_bf16_f32 v89, v119, v89
	v_cndmask_b32_e64 v90, 0, v90, s[0:1]
	ds_read_b128 v[116:119], v125 offset:9248
	s_waitcnt lgkmcnt(1)
	v_mfma_f32_32x32x16_bf16 v[66:81], v[82:85], v[86:89], v[66:81]
	v_cmp_le_u32_e64 s[0:1], v120, v115
	s_nop 1
	v_cndmask_b32_e64 v91, 0, v91, s[0:1]
	v_mfma_f32_32x32x16_bf16 v[50:65], v[82:85], v[98:101], v[50:65]
	v_or_b32_e32 v82, 18, v124
	v_cmp_le_u32_e64 s[0:1], v82, v115
	v_or_b32_e32 v82, 19, v124
	s_nop 0
	v_cndmask_b32_e64 v83, 0, v92, s[0:1]
	v_cmp_le_u32_e64 s[0:1], v82, v115
	v_or_b32_e32 v82, 24, v124
	v_mfma_f32_32x32x16_bf16 v[34:49], v[102:105], v[86:89], v[34:49]
	v_cndmask_b32_e64 v84, 0, v93, s[0:1]
	v_cmp_le_u32_e64 s[0:1], v82, v115
	v_or_b32_e32 v82, 25, v124
	v_cvt_pk_bf16_f32 v83, v83, v84
	v_cndmask_b32_e64 v85, 0, v94, s[0:1]
	v_cmp_le_u32_e64 s[0:1], v82, v115
	v_or_b32_e32 v82, 26, v124
	v_mfma_f32_32x32x16_bf16 v[2:17], v[102:105], v[98:101], v[2:17]
	v_cndmask_b32_e64 v86, 0, v95, s[0:1]
	v_cmp_le_u32_e64 s[0:1], v82, v115
	v_or_b32_e32 v82, 27, v124
	v_cvt_pk_bf16_f32 v84, v85, v86
	v_cndmask_b32_e64 v87, 0, v96, s[0:1]
	v_cmp_le_u32_e64 s[0:1], v82, v115
	v_cvt_pk_bf16_f32 v82, v90, v91
	ds_read_b128 v[90:93], v125 offset:13856
	v_cndmask_b32_e64 v88, 0, v97, s[0:1]
	v_cvt_pk_bf16_f32 v85, v87, v88
	v_or_b32_e32 v94, 32, v115
	v_or_b32_e32 v95, 33, v124
	s_waitcnt lgkmcnt(1)
	v_mfma_f32_32x32x16_bf16 v[66:81], v[116:119], v[82:85], v[66:81]
	v_cvt_pk_bf16_f32 v86, v106, v107
	v_cvt_pk_bf16_f32 v87, v108, v109
	v_cvt_pk_bf16_f32 v88, v110, v111
	v_cvt_pk_bf16_f32 v89, v112, v113
	v_or_b32_e32 v96, 34, v124
	v_cmp_le_u32_e32 vcc, v95, v94
	v_or_b32_e32 v97, 35, v124
	s_waitcnt lgkmcnt(0)
; #define R2_ZERO(M) do { _Pragma("unroll") for (int _a = 0; _a < 2; ++_a) _Pragma("unroll") for (int _b = 0; _b < 2; ++_b) _Pragma("unroll") for (int _r = 0; _r < 16; ++_r) M[_a][_b][_r] = 0.f; } while (0)
; #define R2_RELANE() do { lane = lt_tid(wvid) & 63; l31 = lane & 31; hi = lane >> 5; } while (0)
; __device__ __forceinline__ void ph_rwkv_chunk(const Params& p, int l, LAS unsigned char* lds, const int wvid) {
;     ...
;             M64 Yl; R2_ZERO(Yl); R2_MM_LP(Yl, X, ABR); R2_MM_LP(Yl, Y, AKR);
;             R2_STORE_T(YLg, Yl, false, 1.0f);
;         }
;         R2_RELANE();
;         {
;             M64 Q; R2_ZERO(Q);
;             { bf16x8 Bp[4][2]; R2_PSEUDO(Bp, BTg); R2_MM_LP(Q, X, Bp); }
	v_mfma_f32_32x32x16_bf16 v[34:49], v[90:93], v[82:85], v[34:49]
	ds_read_b128 v[82:85], v125 offset:9280
	v_cndmask_b32_e32 v19, 0, v19, vcc
	v_cmp_le_u32_e32 vcc, v96, v94
	v_or_b32_e32 v98, 40, v124
	v_or_b32_e32 v99, 41, v124
	v_cndmask_b32_e32 v20, 0, v20, vcc
	v_cmp_le_u32_e32 vcc, v97, v94
	v_mfma_f32_32x32x16_bf16 v[50:65], v[116:119], v[86:89], v[50:65]
	v_or_b32_e32 v100, 42, v124
	v_cndmask_b32_e32 v21, 0, v21, vcc
	v_cmp_le_u32_e32 vcc, v98, v94
	v_or_b32_e32 v101, 43, v124
	v_cvt_pk_bf16_f32 v18, v18, v19
	v_cndmask_b32_e32 v22, 0, v22, vcc
	v_cmp_le_u32_e32 vcc, v99, v94
	v_mfma_f32_32x32x16_bf16 v[2:17], v[90:93], v[86:89], v[2:17]
	v_cvt_pk_bf16_f32 v19, v20, v21
	v_cndmask_b32_e32 v23, 0, v23, vcc
	v_cmp_le_u32_e32 vcc, v100, v94
	v_cvt_pk_bf16_f32 v20, v22, v23
	v_or_b32_e32 v86, 48, v124
	v_cndmask_b32_e32 v24, 0, v24, vcc
	v_cmp_le_u32_e32 vcc, v101, v94
	s_waitcnt lgkmcnt(0)
	v_mfma_f32_32x32x16_bf16 v[66:81], v[82:85], v[130:133], v[66:81]
	v_or_b32_e32 v87, 49, v124
	v_cndmask_b32_e32 v25, 0, v25, vcc
	v_cvt_pk_bf16_f32 v21, v24, v25
	v_cmp_le_u32_e32 vcc, v86, v94
	v_or_b32_e32 v88, 50, v124
	v_or_b32_e32 v89, 51, v124
	v_cndmask_b32_e32 v26, 0, v26, vcc
	v_mfma_f32_32x32x16_bf16 v[50:65], v[82:85], v[18:21], v[50:65]
	ds_read_b128 v[22:25], v125 offset:13888
	ds_read_b128 v[82:85], v125 offset:9312
	v_cmp_le_u32_e32 vcc, v87, v94
	v_or_b32_e32 v90, 56, v124
	v_or_b32_e32 v91, 57, v124
	v_cndmask_b32_e32 v27, 0, v27, vcc
	v_cmp_le_u32_e32 vcc, v88, v94
	v_or_b32_e32 v92, 58, v124
	s_waitcnt lgkmcnt(1)
	v_mfma_f32_32x32x16_bf16 v[2:17], v[22:25], v[18:21], v[2:17]
	v_cndmask_b32_e32 v19, 0, v28, vcc
	v_cmp_le_u32_e32 vcc, v89, v94
	v_or_b32_e32 v93, 59, v124
	v_cvt_pk_bf16_f32 v18, v26, v27
	v_cndmask_b32_e32 v20, 0, v29, vcc
	v_cmp_le_u32_e32 vcc, v90, v94
	v_cvt_pk_bf16_f32 v19, v19, v20
	v_mfma_f32_32x32x16_bf16 v[34:49], v[22:25], v[130:133], v[34:49]
	v_cndmask_b32_e32 v21, 0, v30, vcc
	v_cmp_le_u32_e32 vcc, v91, v94
	s_add_u32 s0, s81, s38
	s_addc_u32 s1, s58, s39
	v_cndmask_b32_e32 v22, 0, v31, vcc
	v_cmp_le_u32_e32 vcc, v92, v94
	v_cvt_pk_bf16_f32 v20, v21, v22
	s_waitcnt lgkmcnt(0)
	v_mfma_f32_32x32x16_bf16 v[66:81], v[82:85], v[130:133], v[66:81]
	v_cndmask_b32_e32 v23, 0, v32, vcc
	v_cmp_le_u32_e32 vcc, v93, v94
	s_nop 1
	v_cndmask_b32_e32 v24, 0, v33, vcc
	v_cvt_pk_bf16_f32 v21, v23, v24
	ds_read_b128 v[22:25], v125 offset:13920
	s_waitcnt lgkmcnt(0)
	v_mfma_f32_32x32x16_bf16 v[34:49], v[22:25], v[130:133], v[34:49]
	v_mfma_f32_32x32x16_bf16 v[50:65], v[82:85], v[18:21], v[50:65]
	v_mfma_f32_32x32x16_bf16 v[2:17], v[22:25], v[18:21], v[2:17]
	s_nop 0
	v_cvt_pk_bf16_f32 v18, v66, v67
	v_cvt_pk_bf16_f32 v19, v68, v69
	v_cvt_pk_bf16_f32 v20, v70, v71
	v_cvt_pk_bf16_f32 v21, v72, v73
	s_nop 0
	v_permlane32_swap_b32_e32 v18, v20
	v_permlane32_swap_b32_e32 v19, v21
	global_store_dwordx4 v0, v[18:21], s[0:1]
	v_lshl_add_u64 v[22:23], s[0:1], 0, v[0:1]
	v_add_co_u32_e32 v22, vcc, s44, v22
	v_cvt_pk_bf16_f32 v18, v74, v75
	v_cvt_pk_bf16_f32 v19, v76, v77
	v_cvt_pk_bf16_f32 v20, v78, v79
	v_cvt_pk_bf16_f32 v21, v80, v81
	s_nop 0
	v_permlane32_swap_b32_e32 v18, v20
	v_permlane32_swap_b32_e32 v19, v21
	global_store_dwordx4 v0, v[18:21], s[0:1] offset:2048
	v_cvt_pk_bf16_f32 v2, v2, v3
	v_cvt_pk_bf16_f32 v3, v4, v5
	v_cvt_pk_bf16_f32 v18, v50, v51
	v_cvt_pk_bf16_f32 v19, v52, v53
	v_cvt_pk_bf16_f32 v20, v54, v55
	v_cvt_pk_bf16_f32 v21, v56, v57
	s_nop 0
	v_permlane32_swap_b32_e32 v18, v20
	v_permlane32_swap_b32_e32 v19, v21
	global_store_dwordx4 v0, v[18:21], s[0:1] offset:1024
	v_cvt_pk_bf16_f32 v4, v6, v7
	v_cvt_pk_bf16_f32 v5, v8, v9
	v_cvt_pk_bf16_f32 v18, v58, v59
	v_cvt_pk_bf16_f32 v19, v60, v61
	v_cvt_pk_bf16_f32 v20, v62, v63
	v_cvt_pk_bf16_f32 v21, v64, v65
	s_nop 0
	v_permlane32_swap_b32_e32 v18, v20
	v_permlane32_swap_b32_e32 v19, v21
	global_store_dwordx4 v0, v[18:21], s[0:1] offset:3072
	v_addc_co_u32_e32 v23, vcc, 0, v23, vcc
	s_nop 0
	v_cvt_pk_bf16_f32 v18, v34, v35
	v_cvt_pk_bf16_f32 v19, v36, v37
	v_cvt_pk_bf16_f32 v20, v38, v39
	v_cvt_pk_bf16_f32 v21, v40, v41
	s_nop 0
	v_permlane32_swap_b32_e32 v18, v20
	v_permlane32_swap_b32_e32 v19, v21
	v_permlane32_swap_b32_e32 v2, v4
	v_permlane32_swap_b32_e32 v3, v5
	global_store_dwordx4 v[22:23], v[18:21], off
	global_store_dwordx4 v[22:23], v[2:5], off offset:1024
	s_movk_i32 s0, 0x400
	v_cvt_pk_bf16_f32 v18, v42, v43
	v_cvt_pk_bf16_f32 v19, v44, v45
	v_cvt_pk_bf16_f32 v20, v46, v47
	v_cvt_pk_bf16_f32 v21, v48, v49
	v_cvt_pk_bf16_f32 v2, v10, v11
	v_cvt_pk_bf16_f32 v3, v12, v13
	v_cvt_pk_bf16_f32 v4, v14, v15
	v_cvt_pk_bf16_f32 v5, v16, v17
	v_permlane32_swap_b32_e32 v18, v20
	v_permlane32_swap_b32_e32 v19, v21
	v_permlane32_swap_b32_e32 v2, v4
	v_permlane32_swap_b32_e32 v3, v5
	global_store_dwordx4 v[22:23], v[18:21], off offset:2048
	global_store_dwordx4 v[22:23], v[2:5], off offset:3072
	v_mbcnt_lo_u32_b32 v71, -1, 0
	v_mbcnt_hi_u32_b32 v71, -1, v71
	s_nop 0
	v_bfe_u32 v69, v71, 5, 1
	v_lshlrev_b32_e32 v0, 6, v71
	v_and_b32_e32 v2, 15, v71
	v_lshlrev_b32_e32 v3, 6, v69
	v_and_or_b32 v0, v0, s0, v2
	v_lshl_or_b32 v70, v69, 2, 2
	v_or_b32_e32 v7, 0x80, v3
	v_or_b32_e32 v9, 0xa0, v3
	v_or_b32_e32 v4, v0, v3
	v_lshlrev_b32_e32 v5, 4, v70
	v_or_b32_e32 v8, v7, v0
	v_or_b32_e32 v10, v9, v0
	v_lshlrev_b32_e32 v4, 1, v4
	v_or_b32_e32 v6, v5, v0
	v_lshlrev_b32_e32 v8, 1, v8
	v_lshlrev_b32_e32 v10, 1, v10
	v_or_b32_e32 v2, 0x800, v0
	v_lshlrev_b32_e32 v6, 1, v6
	global_load_ushort v11, v4, s[70:71]
	global_load_ushort v12, v4, s[70:71] offset:32
	global_load_ushort v13, v6, s[70:71]
	global_load_ushort v14, v6, s[70:71] offset:32
	global_load_ushort v15, v8, s[70:71]
; __device__ __forceinline__ void ph_rwkv_chunk(const Params& p, int l, LAS unsigned char* lds, const int wvid) {
;     ...
;             { bf16x8 Bp[4][2]; R2_PSEUDO(Bp, BTg); R2_MM_LP(Q, X, Bp); }
	s_nop 0
	global_load_ushort v8, v8, s[70:71] offset:32
	s_nop 0
	global_load_ushort v16, v10, s[70:71]
	s_nop 0
	global_load_ushort v10, v10, s[70:71] offset:32
	v_or_b32_e32 v4, 0x810, v0
	v_or_b32_e32 v6, v2, v3
	v_or_b32_e32 v17, v4, v3
	v_or_b32_e32 v18, v2, v5
	v_or_b32_e32 v19, v2, v7
	v_or_b32_e32 v20, v2, v9
	v_lshlrev_b32_e32 v6, 1, v6
	v_lshlrev_b32_e32 v17, 1, v17
	v_lshlrev_b32_e32 v18, 1, v18
	v_or_b32_e32 v5, v4, v5
	v_lshlrev_b32_e32 v19, 1, v19
	v_or_b32_e32 v7, v4, v7
	v_lshlrev_b32_e32 v20, 1, v20
	v_or_b32_e32 v9, v4, v9
	v_lshlrev_b32_e32 v5, 1, v5
	v_lshlrev_b32_e32 v7, 1, v7
	v_lshlrev_b32_e32 v9, 1, v9
	global_load_ushort v21, v6, s[70:71]
	s_nop 0
	global_load_ushort v17, v17, s[70:71]
	s_nop 0
	global_load_ushort v18, v18, s[70:71]
	s_nop 0
	global_load_ushort v22, v5, s[70:71]
	s_nop 0
	global_load_ushort v19, v19, s[70:71]
	s_nop 0
	global_load_ushort v23, v7, s[70:71]
	s_nop 0
	global_load_ushort v20, v20, s[70:71]
	s_nop 0
	global_load_ushort v24, v9, s[70:71]
	v_or_b32_e32 v5, 0x100, v3
	v_or_b32_e32 v6, v5, v0
	v_or_b32_e32 v7, 0x120, v3
	v_or_b32_e32 v25, 0x180, v3
	v_or_b32_e32 v27, 0x1a0, v3
	v_lshlrev_b32_e32 v6, 1, v6
	v_or_b32_e32 v9, v7, v0
	v_or_b32_e32 v26, v25, v0
	v_or_b32_e32 v28, v27, v0
	v_lshlrev_b32_e32 v9, 1, v9
	v_lshlrev_b32_e32 v26, 1, v26
	v_lshlrev_b32_e32 v28, 1, v28
	global_load_ushort v76, v6, s[70:71]
	global_load_ushort v77, v6, s[70:71] offset:32
	global_load_ushort v78, v9, s[70:71]
	global_load_ushort v79, v9, s[70:71] offset:32
	global_load_ushort v80, v26, s[70:71]
	global_load_ushort v81, v26, s[70:71] offset:32
	global_load_ushort v82, v28, s[70:71]
	global_load_ushort v83, v28, s[70:71] offset:32
	v_or_b32_e32 v6, v2, v5
	v_lshlrev_b32_e32 v6, 1, v6
	v_or_b32_e32 v5, v4, v5
	v_or_b32_e32 v9, v2, v7
	v_or_b32_e32 v7, v4, v7
	v_or_b32_e32 v26, v2, v25
	v_or_b32_e32 v25, v4, v25
	v_or_b32_e32 v28, v2, v27
	v_or_b32_e32 v27, v4, v27
	v_lshlrev_b32_e32 v5, 1, v5
	v_lshlrev_b32_e32 v9, 1, v9
	v_lshlrev_b32_e32 v7, 1, v7
	v_lshlrev_b32_e32 v26, 1, v26
	v_lshlrev_b32_e32 v25, 1, v25
	v_lshlrev_b32_e32 v28, 1, v28
	v_lshlrev_b32_e32 v27, 1, v27
	global_load_ushort v84, v6, s[70:71]
	global_load_ushort v85, v5, s[70:71]
	global_load_ushort v86, v9, s[70:71]
	global_load_ushort v87, v7, s[70:71]
	global_load_ushort v88, v26, s[70:71]
	global_load_ushort v89, v25, s[70:71]
	global_load_ushort v90, v28, s[70:71]
	global_load_ushort v91, v27, s[70:71]
	v_or_b32_e32 v5, 0x200, v3
	v_or_b32_e32 v6, v5, v0
	v_or_b32_e32 v7, 0x220, v3
	v_or_b32_e32 v25, 0x280, v3
	v_or_b32_e32 v27, 0x2a0, v3
	v_lshlrev_b32_e32 v6, 1, v6
	v_or_b32_e32 v9, v7, v0
	v_or_b32_e32 v26, v25, v0
	v_or_b32_e32 v28, v27, v0
	v_lshlrev_b32_e32 v9, 1, v9
	v_lshlrev_b32_e32 v26, 1, v26
	v_lshlrev_b32_e32 v28, 1, v28
	global_load_ushort v92, v6, s[70:71]
	global_load_ushort v93, v6, s[70:71] offset:32
	global_load_ushort v94, v9, s[70:71]
	global_load_ushort v95, v9, s[70:71] offset:32
	global_load_ushort v96, v26, s[70:71]
	global_load_ushort v97, v26, s[70:71] offset:32
	global_load_ushort v98, v28, s[70:71]
	global_load_ushort v99, v28, s[70:71] offset:32
	v_or_b32_e32 v6, v2, v5
	v_lshlrev_b32_e32 v6, 1, v6
	v_or_b32_e32 v5, v4, v5
	v_or_b32_e32 v9, v2, v7
	v_or_b32_e32 v7, v4, v7
	v_or_b32_e32 v26, v2, v25
	v_or_b32_e32 v25, v4, v25
	v_or_b32_e32 v28, v2, v27
	v_or_b32_e32 v27, v4, v27
	v_lshlrev_b32_e32 v5, 1, v5
	v_lshlrev_b32_e32 v9, 1, v9
	v_lshlrev_b32_e32 v7, 1, v7
	v_lshlrev_b32_e32 v26, 1, v26
	v_lshlrev_b32_e32 v25, 1, v25
	v_lshlrev_b32_e32 v28, 1, v28
	v_lshlrev_b32_e32 v27, 1, v27
	global_load_ushort v100, v6, s[70:71]
	global_load_ushort v101, v5, s[70:71]
	global_load_ushort v102, v9, s[70:71]
	global_load_ushort v103, v7, s[70:71]
	global_load_ushort v104, v26, s[70:71]
	global_load_ushort v105, v25, s[70:71]
	global_load_ushort v106, v28, s[70:71]
	global_load_ushort v107, v27, s[70:71]
	v_or_b32_e32 v5, 0x300, v3
	v_or_b32_e32 v7, 0x320, v3
	v_or_b32_e32 v25, 0x380, v3
	v_or_b32_e32 v3, 0x3a0, v3
	v_or_b32_e32 v6, v5, v0
	v_or_b32_e32 v9, v7, v0
	v_or_b32_e32 v26, v25, v0
	v_or_b32_e32 v0, v3, v0
	v_lshlrev_b32_e32 v6, 1, v6
	v_lshlrev_b32_e32 v0, 1, v0
	v_lshlrev_b32_e32 v9, 1, v9
	v_lshlrev_b32_e32 v26, 1, v26
	global_load_ushort v108, v6, s[70:71]
	global_load_ushort v109, v6, s[70:71] offset:32
	global_load_ushort v110, v9, s[70:71]
	global_load_ushort v111, v9, s[70:71] offset:32
	global_load_ushort v112, v26, s[70:71]
	global_load_ushort v113, v26, s[70:71] offset:32
	global_load_ushort v114, v0, s[70:71]
	s_nop 0
	global_load_ushort v0, v0, s[70:71] offset:32
	v_or_b32_e32 v6, v2, v5
	v_lshlrev_b32_e32 v6, 1, v6
	v_or_b32_e32 v5, v4, v5
	v_or_b32_e32 v9, v2, v7
	v_or_b32_e32 v7, v4, v7
	v_or_b32_e32 v26, v2, v25
	v_or_b32_e32 v25, v4, v25
	v_or_b32_e32 v2, v2, v3
	v_or_b32_e32 v3, v4, v3
	v_lshlrev_b32_e32 v5, 1, v5
	v_lshlrev_b32_e32 v9, 1, v9
	v_lshlrev_b32_e32 v7, 1, v7
	v_lshlrev_b32_e32 v26, 1, v26
	v_lshlrev_b32_e32 v25, 1, v25
	v_lshlrev_b32_e32 v2, 1, v2
	v_lshlrev_b32_e32 v3, 1, v3
	global_load_ushort v115, v6, s[70:71]
	global_load_ushort v116, v5, s[70:71]
	global_load_ushort v117, v9, s[70:71]
	global_load_ushort v118, v7, s[70:71]
	global_load_ushort v119, v26, s[70:71]
	global_load_ushort v120, v25, s[70:71]
	global_load_ushort v121, v2, s[70:71]
	global_load_ushort v122, v3, s[70:71]
	v_and_b32_e32 v66, 31, v71
	v_lshlrev_b32_e32 v67, 4, v69
	v_mul_u32_u24_e32 v2, 0x90, v66
	v_add3_u32 v68, s48, v67, v2
	ds_read_b128 v[2:5], v68
	ds_read_b128 v[72:75], v68 offset:32
	s_waitcnt vmcnt(62)
	v_lshl_or_b32 v6, v12, 16, v11
	s_waitcnt vmcnt(60)
	v_lshl_or_b32 v7, v14, 16, v13
	s_waitcnt vmcnt(58)
; __device__ __forceinline__ void ph_rwkv_chunk(const Params& p, int l, LAS unsigned char* lds, const int wvid) {
;     ...
;             { bf16x8 Bp[4][2]; R2_PSEUDO(Bp, BTg); R2_MM_LP(Q, X, Bp); }
;             { bf16x8 Kp[4][2]; asm volatile("" ::: "memory"); R2_RAW(X, KTg); R2_PSEUDO_L(Kp, X); R2_MM_LP(Q, Y, Kp); }
	v_lshl_or_b32 v8, v8, 16, v15
	s_waitcnt vmcnt(56)
	v_lshl_or_b32 v9, v10, 16, v16
	s_waitcnt vmcnt(54)
	v_lshl_or_b32 v10, v17, 16, v21
	s_waitcnt vmcnt(52)
	v_lshl_or_b32 v11, v22, 16, v18
	s_waitcnt vmcnt(50)
	v_lshl_or_b32 v12, v23, 16, v19
	s_waitcnt vmcnt(48)
	v_lshl_or_b32 v13, v24, 16, v20
	s_waitcnt lgkmcnt(1)
	v_mfma_f32_32x32x16_bf16 v[34:49], v[2:5], v[6:9], 0
	s_waitcnt vmcnt(46)
	v_lshl_or_b32 v76, v77, 16, v76
	s_waitcnt vmcnt(44)
	v_lshl_or_b32 v77, v79, 16, v78
	s_waitcnt vmcnt(42)
	v_lshl_or_b32 v78, v81, 16, v80
	s_waitcnt vmcnt(40)
	v_lshl_or_b32 v79, v83, 16, v82
	s_waitcnt vmcnt(38)
	v_lshl_or_b32 v80, v85, 16, v84
	s_waitcnt vmcnt(36)
	v_lshl_or_b32 v81, v87, 16, v86
	s_waitcnt vmcnt(34)
	v_lshl_or_b32 v82, v89, 16, v88
	v_mfma_f32_32x32x16_bf16 v[50:65], v[2:5], v[10:13], 0
	ds_read_b128 v[2:5], v68 offset:4608
	s_waitcnt vmcnt(32)
	v_lshl_or_b32 v83, v91, 16, v90
	v_mul_u32_u24_e32 v69, 0x240, v69
	v_mul_u32_u24_e32 v70, 0x90, v70
	s_movk_i32 s70, 0x1000
	s_waitcnt lgkmcnt(1)
	v_mfma_f32_32x32x16_bf16 v[34:49], v[72:75], v[76:79], v[34:49]
	v_mfma_f32_32x32x16_bf16 v[50:65], v[72:75], v[80:83], v[50:65]
	ds_read_b128 v[72:75], v68 offset:4640
	s_waitcnt lgkmcnt(1)
	v_mfma_f32_32x32x16_bf16 v[18:33], v[2:5], v[6:9], 0
	v_mfma_f32_32x32x16_bf16 v[2:17], v[2:5], v[10:13], 0
	s_waitcnt lgkmcnt(0)
	v_mfma_f32_32x32x16_bf16 v[18:33], v[72:75], v[76:79], v[18:33]
	s_waitcnt vmcnt(30)
	v_lshl_or_b32 v76, v93, 16, v92
	s_waitcnt vmcnt(28)
	v_lshl_or_b32 v77, v95, 16, v94
	s_waitcnt vmcnt(26)
	v_lshl_or_b32 v78, v97, 16, v96
	s_waitcnt vmcnt(24)
	v_lshl_or_b32 v79, v99, 16, v98
	v_mfma_f32_32x32x16_bf16 v[2:17], v[72:75], v[80:83], v[2:17]
	ds_read_b128 v[72:75], v68 offset:64
	s_waitcnt vmcnt(22)
	v_lshl_or_b32 v80, v101, 16, v100
	s_waitcnt vmcnt(20)
	v_lshl_or_b32 v81, v103, 16, v102
	s_waitcnt vmcnt(18)
	v_lshl_or_b32 v82, v105, 16, v104
	s_waitcnt vmcnt(16)
	v_lshl_or_b32 v83, v107, 16, v106
	s_waitcnt lgkmcnt(0)
	v_mfma_f32_32x32x16_bf16 v[34:49], v[72:75], v[76:79], v[34:49]
	v_mfma_f32_32x32x16_bf16 v[50:65], v[72:75], v[80:83], v[50:65]
	ds_read_b128 v[72:75], v68 offset:4672
	s_waitcnt lgkmcnt(0)
	v_mfma_f32_32x32x16_bf16 v[18:33], v[72:75], v[76:79], v[18:33]
	s_waitcnt vmcnt(14)
	v_lshl_or_b32 v76, v109, 16, v108
	s_waitcnt vmcnt(12)
	v_lshl_or_b32 v77, v111, 16, v110
	s_waitcnt vmcnt(10)
	v_lshl_or_b32 v78, v113, 16, v112
	s_waitcnt vmcnt(8)
	v_lshl_or_b32 v79, v0, 16, v114
	v_and_b32_e32 v0, 63, v71
	v_lshlrev_b32_e32 v0, 4, v0
	v_lshl_add_u64 v[96:97], s[36:37], 0, v[0:1]
	v_mfma_f32_32x32x16_bf16 v[2:17], v[72:75], v[80:83], v[2:17]
	ds_read_b128 v[72:75], v68 offset:96
	s_waitcnt vmcnt(6)
	v_lshl_or_b32 v80, v116, 16, v115
	s_waitcnt vmcnt(4)
	v_lshl_or_b32 v81, v118, 16, v117
	s_waitcnt vmcnt(2)
	v_lshl_or_b32 v82, v120, 16, v119
	s_waitcnt vmcnt(0)
	v_lshl_or_b32 v83, v122, 16, v121
	v_add_co_u32_e32 v108, vcc, s44, v96
	s_waitcnt lgkmcnt(0)
	v_mfma_f32_32x32x16_bf16 v[34:49], v[72:75], v[76:79], v[34:49]
	v_addc_co_u32_e32 v109, vcc, 0, v97, vcc
	v_mfma_f32_32x32x16_bf16 v[50:65], v[72:75], v[80:83], v[50:65]
	ds_read_b128 v[72:75], v68 offset:4704
	s_waitcnt lgkmcnt(0)
	v_mfma_f32_32x32x16_bf16 v[18:33], v[72:75], v[76:79], v[18:33]
	global_load_dwordx4 v[76:79], v0, s[36:37]
	global_load_dwordx4 v[84:87], v0, s[36:37] offset:1024
	global_load_dwordx4 v[88:91], v0, s[36:37] offset:2048
	global_load_dwordx4 v[92:95], v0, s[36:37] offset:3072
	global_load_dwordx4 v[96:99], v[108:109], off
	global_load_dwordx4 v[100:103], v[108:109], off offset:1024
	global_load_dwordx4 v[104:107], v[108:109], off offset:2048
	s_nop 0
	global_load_dwordx4 v[108:111], v[108:109], off offset:3072
	v_lshlrev_b32_e32 v0, 4, v71
	v_bfe_u32 v71, v71, 1, 5
	v_and_b32_e32 v0, 16, v0
	v_mul_u32_u24_e32 v71, 0x90, v71
	v_add3_u32 v0, s48, v71, v0
	s_waitcnt vmcnt(7)
	ds_write_b128 v0, v[76:79]
	s_waitcnt vmcnt(6)
	ds_write_b128 v0, v[84:87] offset:4608
	s_waitcnt vmcnt(5)
	ds_write_b128 v0, v[88:91] offset:32
	s_waitcnt vmcnt(4)
	ds_write_b128 v0, v[92:95] offset:4640
	s_waitcnt vmcnt(3)
	ds_write_b128 v0, v[96:99] offset:64
	s_waitcnt vmcnt(2)
	ds_write_b128 v0, v[100:103] offset:4672
	s_waitcnt vmcnt(1)
	ds_write_b128 v0, v[104:107] offset:96
	s_waitcnt vmcnt(0)
	ds_write_b128 v0, v[108:111] offset:4704
	v_lshlrev_b32_e32 v0, 1, v66
	v_add3_u32 v69, s48, v69, v0
	v_add3_u32 v0, s48, v70, v0
	v_mfma_f32_32x32x16_bf16 v[2:17], v[72:75], v[80:83], v[2:17]
	ds_read_u16 v74, v69
	ds_read_u16 v75, v69 offset:144
	ds_read_u16 v76, v0
	ds_read_u16 v77, v0 offset:144
	ds_read_u16 v79, v0 offset:208
	ds_read_u16 v80, v0 offset:64
	ds_read_u16 v78, v69 offset:208
	ds_read_u16 v69, v69 offset:64
	ds_read_u16 v81, v0 offset:864
	ds_read_u16 v82, v0 offset:1008
	ds_read_u16 v83, v0 offset:1152
	ds_read_u16 v84, v0 offset:1296
	ds_read_u16 v85, v0 offset:1360
	ds_read_u16 v86, v0 offset:1216
	ds_read_u16 v87, v0 offset:1072
	ds_read_u16 v88, v0 offset:928
	ds_read_u16 v89, v0 offset:2016
	ds_read_u16 v90, v0 offset:2160
	ds_read_u16 v91, v0 offset:2304
	ds_read_u16 v92, v0 offset:2448
	ds_read_u16 v93, v0 offset:2512
	ds_read_u16 v94, v0 offset:2368
	ds_read_u16 v95, v0 offset:2224
	ds_read_u16 v96, v0 offset:2080
	ds_read_u16 v97, v0 offset:3168
	ds_read_u16 v98, v0 offset:3312
	ds_read_u16 v99, v0 offset:3456
	ds_read_u16 v100, v0 offset:3600
	ds_read_u16 v101, v0 offset:3664
	ds_read_u16 v102, v0 offset:3520
	ds_read_u16 v103, v0 offset:3376
	ds_read_u16 v104, v0 offset:3232
	ds_read_u16 v105, v0 offset:4320
	ds_read_u16 v106, v0 offset:4464
	ds_read_u16 v107, v0 offset:4608
	ds_read_u16 v108, v0 offset:4752
	ds_read_u16 v109, v0 offset:4816
	ds_read_u16 v110, v0 offset:4672
	ds_read_u16 v111, v0 offset:4528
	ds_read_u16 v112, v0 offset:4384
	ds_read_u16 v113, v0 offset:5472
	ds_read_u16 v114, v0 offset:5616
	ds_read_u16 v115, v0 offset:5760
	ds_read_u16 v116, v0 offset:5904
	ds_read_u16 v117, v0 offset:5968
	ds_read_u16 v118, v0 offset:5824
	ds_read_u16 v119, v0 offset:5680
	ds_read_u16 v120, v0 offset:5536
	ds_read_u16 v121, v0 offset:6624
	ds_read_u16 v122, v0 offset:6768
	ds_read_u16 v123, v0 offset:6912
	ds_read_u16 v124, v0 offset:7056
	ds_read_u16 v125, v0 offset:7120
	ds_read_u16 v126, v0 offset:6976
	ds_read_u16 v127, v0 offset:6832
	ds_read_u16 v128, v0 offset:6688
	ds_read_u16 v129, v0 offset:7776
	ds_read_u16 v130, v0 offset:7920
	ds_read_u16 v131, v0 offset:8064
	ds_read_u16 v132, v0 offset:8208
	ds_read_u16 v133, v0 offset:8272
	ds_read_u16 v134, v0 offset:8128
	ds_read_u16 v135, v0 offset:7984
	ds_read_u16 v0, v0 offset:7840
	ds_read_b128 v[70:73], v68 offset:9216
	s_waitcnt lgkmcnt(14)
; __device__ __forceinline__ void ph_rwkv_chunk(const Params& p, int l, LAS unsigned char* lds, const int wvid) {
;     ...
;             { bf16x8 Kp[4][2]; asm volatile("" ::: "memory"); R2_RAW(X, KTg); R2_PSEUDO_L(Kp, X); R2_MM_LP(Q, Y, Kp); }
; #pragma unroll
;             for (int rb = 0; rb < 2; ++rb)
; #pragma unroll
;                 for (int r = 0; r < 16; ++r) { Q[rb][0][r] *= gc0; Q[rb][1][r] *= gc1; }
;             R2_STORE_T(QTg, Q, false, 1.0f);
	v_lshl_or_b32 v74, v75, 16, v74
	v_lshl_or_b32 v75, v77, 16, v76
	v_lshl_or_b32 v76, v82, 16, v81
	v_lshl_or_b32 v77, v84, 16, v83
	v_lshl_or_b32 v78, v78, 16, v69
	v_lshl_or_b32 v79, v79, 16, v80
	v_lshl_or_b32 v80, v87, 16, v88
	v_lshl_or_b32 v81, v85, 16, v86
	s_waitcnt lgkmcnt(0)
	v_mfma_f32_32x32x16_bf16 v[34:49], v[70:73], v[74:77], v[34:49]
	v_mfma_f32_32x32x16_bf16 v[50:65], v[70:73], v[78:81], v[50:65]
	ds_read_b128 v[70:73], v68 offset:13824
	s_waitcnt lgkmcnt(0)
	v_mfma_f32_32x32x16_bf16 v[18:33], v[70:73], v[74:77], v[18:33]
	v_lshl_or_b32 v74, v90, 16, v89
	v_lshl_or_b32 v75, v92, 16, v91
	v_lshl_or_b32 v76, v98, 16, v97
	v_lshl_or_b32 v77, v100, 16, v99
	v_mfma_f32_32x32x16_bf16 v[2:17], v[70:73], v[78:81], v[2:17]
	ds_read_b128 v[70:73], v68 offset:9248
	v_lshl_or_b32 v78, v95, 16, v96
	v_lshl_or_b32 v79, v93, 16, v94
	v_lshl_or_b32 v80, v103, 16, v104
	v_lshl_or_b32 v81, v101, 16, v102
	s_waitcnt lgkmcnt(0)
	v_mfma_f32_32x32x16_bf16 v[34:49], v[70:73], v[74:77], v[34:49]
	v_mfma_f32_32x32x16_bf16 v[50:65], v[70:73], v[78:81], v[50:65]
	ds_read_b128 v[70:73], v68 offset:13856
	s_waitcnt lgkmcnt(0)
	v_mfma_f32_32x32x16_bf16 v[18:33], v[70:73], v[74:77], v[18:33]
	v_lshl_or_b32 v74, v106, 16, v105
	v_lshl_or_b32 v75, v108, 16, v107
	v_lshl_or_b32 v76, v114, 16, v113
	v_lshl_or_b32 v77, v116, 16, v115
	v_mfma_f32_32x32x16_bf16 v[2:17], v[70:73], v[78:81], v[2:17]
	ds_read_b128 v[70:73], v68 offset:9280
	v_lshl_or_b32 v78, v111, 16, v112
	v_lshl_or_b32 v79, v109, 16, v110
	v_lshl_or_b32 v80, v119, 16, v120
	v_lshl_or_b32 v81, v117, 16, v118
	s_waitcnt lgkmcnt(0)
	v_mfma_f32_32x32x16_bf16 v[34:49], v[70:73], v[74:77], v[34:49]
	v_mfma_f32_32x32x16_bf16 v[50:65], v[70:73], v[78:81], v[50:65]
	ds_read_b128 v[70:73], v68 offset:13888
	s_waitcnt lgkmcnt(0)
	v_mfma_f32_32x32x16_bf16 v[18:33], v[70:73], v[74:77], v[18:33]
	v_lshl_or_b32 v74, v122, 16, v121
	v_lshl_or_b32 v75, v124, 16, v123
	v_lshl_or_b32 v76, v130, 16, v129
	v_lshl_or_b32 v77, v132, 16, v131
	v_mfma_f32_32x32x16_bf16 v[2:17], v[70:73], v[78:81], v[2:17]
	ds_read_b128 v[70:73], v68 offset:9312
	v_lshl_or_b32 v78, v127, 16, v128
	v_lshl_or_b32 v79, v125, 16, v126
	v_lshl_or_b32 v80, v135, 16, v0
	v_lshl_or_b32 v81, v133, 16, v134
	v_lshl_or_b32 v0, v66, 5, v67
	s_waitcnt lgkmcnt(0)
	v_mfma_f32_32x32x16_bf16 v[34:49], v[70:73], v[74:77], v[34:49]
	v_mfma_f32_32x32x16_bf16 v[50:65], v[70:73], v[78:81], v[50:65]
	ds_read_b128 v[68:71], v68 offset:13920
	s_nop 9
	v_mul_f32_e64 v34, v192, v34
	v_mul_f32_e64 v35, v192, v35
	v_mul_f32_e64 v36, v192, v36
	v_mul_f32_e64 v37, v192, v37
	v_pk_mul_f32 v[38:39], v[192:193], v[38:39] op_sel_hi:[0,1]
	v_pk_mul_f32 v[40:41], v[192:193], v[40:41] op_sel_hi:[0,1]
	v_pk_mul_f32 v[42:43], v[192:193], v[42:43] op_sel_hi:[0,1]
	v_pk_mul_f32 v[44:45], v[192:193], v[44:45] op_sel_hi:[0,1]
	s_waitcnt lgkmcnt(0)
	v_mfma_f32_32x32x16_bf16 v[2:17], v[68:71], v[78:81], v[2:17]
	v_mul_f32_e64 v46, v192, v46
	v_mul_f32_e64 v47, v192, v47
	v_mul_f32_e64 v48, v192, v48
	v_mul_f32_e64 v49, v192, v49
	v_mul_f32_e64 v50, v190, v50
	v_mul_f32_e64 v51, v190, v51
	v_pk_mul_f32 v[52:53], v[190:191], v[52:53] op_sel_hi:[0,1]
	v_pk_mul_f32 v[54:55], v[190:191], v[54:55] op_sel_hi:[0,1]
	v_pk_mul_f32 v[56:57], v[190:191], v[56:57] op_sel_hi:[0,1]
	v_pk_mul_f32 v[58:59], v[190:191], v[58:59] op_sel_hi:[0,1]
	v_mfma_f32_32x32x16_bf16 v[18:33], v[68:71], v[74:77], v[18:33]
	s_nop 0
	v_mul_f32_e64 v68, v190, v2
	v_mul_f32_e64 v69, v190, v3
	v_mul_f32_e64 v70, v190, v4
	v_mul_f32_e64 v71, v190, v5
	v_cvt_pk_bf16_f32 v2, v34, v35
	v_cvt_pk_bf16_f32 v3, v36, v37
	v_cvt_pk_bf16_f32 v4, v38, v39
	v_cvt_pk_bf16_f32 v5, v40, v41
	s_nop 0
	v_permlane32_swap_b32_e32 v2, v4
	v_permlane32_swap_b32_e32 v3, v5
	global_store_dwordx4 v0, v[2:5], s[34:35]
	v_pk_mul_f32 v[60:61], v[190:191], v[60:61] op_sel_hi:[0,1]
	v_pk_mul_f32 v[62:63], v[190:191], v[62:63] op_sel_hi:[0,1]
	v_cvt_pk_bf16_f32 v2, v42, v43
	v_cvt_pk_bf16_f32 v3, v44, v45
	v_cvt_pk_bf16_f32 v4, v46, v47
	v_cvt_pk_bf16_f32 v5, v48, v49
	s_nop 0
	v_permlane32_swap_b32_e32 v2, v4
	v_permlane32_swap_b32_e32 v3, v5
	global_store_dwordx4 v0, v[2:5], s[34:35] offset:2048
	v_pk_mul_f32 v[64:65], v[190:191], v[64:65] op_sel_hi:[0,1]
	v_pk_mul_f32 v[18:19], v[192:193], v[18:19] op_sel_hi:[0,1]
	v_cvt_pk_bf16_f32 v2, v50, v51
	v_cvt_pk_bf16_f32 v3, v52, v53
	v_cvt_pk_bf16_f32 v4, v54, v55
	v_cvt_pk_bf16_f32 v5, v56, v57
	s_nop 0
	v_permlane32_swap_b32_e32 v2, v4
	v_permlane32_swap_b32_e32 v3, v5
	global_store_dwordx4 v0, v[2:5], s[34:35] offset:1024
	v_pk_mul_f32 v[20:21], v[192:193], v[20:21] op_sel_hi:[0,1]
	v_pk_mul_f32 v[22:23], v[192:193], v[22:23] op_sel_hi:[0,1]
	v_cvt_pk_bf16_f32 v2, v58, v59
	v_cvt_pk_bf16_f32 v3, v60, v61
	v_cvt_pk_bf16_f32 v4, v62, v63
	v_cvt_pk_bf16_f32 v5, v64, v65
	v_pk_mul_f32 v[24:25], v[192:193], v[24:25] op_sel_hi:[0,1]
	v_lshl_add_u64 v[34:35], s[34:35], 0, v[0:1]
	v_permlane32_swap_b32_e32 v2, v4
	v_permlane32_swap_b32_e32 v3, v5
	global_store_dwordx4 v0, v[2:5], s[34:35] offset:3072
	v_pk_mul_f32 v[26:27], v[192:193], v[26:27] op_sel_hi:[0,1]
	v_pk_mul_f32 v[28:29], v[192:193], v[28:29] op_sel_hi:[0,1]
	v_cvt_pk_bf16_f32 v2, v18, v19
	v_cvt_pk_bf16_f32 v3, v20, v21
	v_cvt_pk_bf16_f32 v4, v22, v23
	v_cvt_pk_bf16_f32 v5, v24, v25
	v_add_co_u32_e32 v18, vcc, s44, v34
	v_pk_mul_f32 v[30:31], v[192:193], v[30:31] op_sel_hi:[0,1]
	v_pk_mul_f32 v[32:33], v[192:193], v[32:33] op_sel_hi:[0,1]
	v_permlane32_swap_b32_e32 v2, v4
	v_permlane32_swap_b32_e32 v3, v5
	v_addc_co_u32_e32 v19, vcc, 0, v35, vcc
	global_store_dwordx4 v[18:19], v[2:5], off
	v_pk_mul_f32 v[6:7], v[190:191], v[6:7] op_sel_hi:[0,1]
	v_pk_mul_f32 v[8:9], v[190:191], v[8:9] op_sel_hi:[0,1]
	v_cvt_pk_bf16_f32 v2, v26, v27
	v_cvt_pk_bf16_f32 v3, v28, v29
	v_cvt_pk_bf16_f32 v4, v30, v31
	v_cvt_pk_bf16_f32 v5, v32, v33
	s_nop 0
	v_permlane32_swap_b32_e32 v2, v4
	v_permlane32_swap_b32_e32 v3, v5
	global_store_dwordx4 v[18:19], v[2:5], off offset:2048
	v_pk_mul_f32 v[10:11], v[190:191], v[10:11] op_sel_hi:[0,1]
	v_pk_mul_f32 v[12:13], v[190:191], v[12:13] op_sel_hi:[0,1]
	v_cvt_pk_bf16_f32 v2, v68, v69
	v_cvt_pk_bf16_f32 v3, v70, v71
	v_cvt_pk_bf16_f32 v4, v6, v7
	v_cvt_pk_bf16_f32 v5, v8, v9
	v_pk_mul_f32 v[14:15], v[190:191], v[14:15] op_sel_hi:[0,1]
	v_pk_mul_f32 v[16:17], v[190:191], v[16:17] op_sel_hi:[0,1]
	v_permlane32_swap_b32_e32 v2, v4
	v_permlane32_swap_b32_e32 v3, v5
	global_store_dwordx4 v[18:19], v[2:5], off offset:1024
	s_mov_b32 s44, 0x939a85c5
	s_nop 0
	v_cvt_pk_bf16_f32 v2, v10, v11
	v_cvt_pk_bf16_f32 v3, v12, v13
	v_cvt_pk_bf16_f32 v4, v14, v15
	v_cvt_pk_bf16_f32 v5, v16, v17
	s_nop 0
	v_permlane32_swap_b32_e32 v2, v4
	v_permlane32_swap_b32_e32 v3, v5
	global_store_dwordx4 v[18:19], v[2:5], off offset:3072
	s_branch .LBB0_646
